# v5 + P7: inline key codes free 63 VGPRs, both hosted row pairs requested right after the score MFMAs, pair A quantised after 48 insertions
# baseline (speedup 1.0000x reference)
; #define GAS __attribute__((address_space(1)))
; #define LAS __attribute__((address_space(3)))
; DI unsigned pk2(float lo, float hi) { return f2bf(lo) | (f2bf(hi) << 16); }
; DI void p8_phase(Frame& F) {
;     ...
; #pragma unroll 4
;     for (int i = 0; i < 16; ++i) { const int idx = tid * 4 + 2048 * i, side = idx >> 14, rem = idx & 16383, row = rem >> 7, col = rem & 127;
;         const f32x4 a = *(const GAS f32x4*)((side ? F.keys2 : F.keys1) + rem);
;         v2u o; o.x = pk2(a.x, a.y); o.y = pk2(a.z, a.w); *(LAS v2u*)(KIMG + (side * 128 + row) * KPITCH + col * 2) = o; }
.LBB0_1201:
	v_readlane_b32 s4, v252, 4
	v_readlane_b32 s5, v252, 5
	s_cmp_lt_i32 s4, 9
	v_readlane_b32 s4, v252, 13
	s_cselect_b64 s[2:3], -1, 0
	v_readlane_b32 s5, v252, 14
	s_add_u32 s14, s4, 0x3400000
	s_addc_u32 s15, s5, 0
	s_add_u32 s16, s4, 0x2c00000
	s_addc_u32 s17, s5, 0
	s_add_u32 s37, s4, 0x18000000
	s_addc_u32 s39, s5, 0
	s_add_u32 s18, s4, 0x1a000000
	s_addc_u32 s19, s5, 0
	s_add_u32 s20, s4, 0x380000
	s_addc_u32 s21, s5, 0
	s_add_u32 s24, s4, 0x390000
	s_addc_u32 s25, s5, 0
	s_and_b64 s[8:9], s[2:3], s[0:1]
	s_andn2_b64 vcc, exec, s[8:9]
	v_readlane_b32 s6, v252, 6
	v_readlane_b32 s7, v252, 7
	s_cbranch_vccnz .LBB0_1246
	v_lshlrev_b32_e32 v1, 3, v0
	v_lshrrev_b32_e32 v3, 5, v0
	s_waitcnt lgkmcnt(0)
	v_and_b32_e32 v2, 0xf8, v1
	v_or_b32_e32 v1, 48, v3
	v_or_b32_e32 v4, 32, v3
	v_or_b32_e32 v5, 16, v3
	v_mul_u32_u24_e32 v1, 0x110, v1
	v_mul_u32_u24_e32 v4, 0x110, v4
	v_mul_u32_u24_e32 v5, 0x110, v5
	v_mul_u32_u24_e32 v3, 0x110, v3
	s_mov_b32 s2, 0
	v_add3_u32 v1, v1, v2, 0
	v_add3_u32 v4, v4, v2, 0
	v_add3_u32 v5, v5, v2, 0
	v_add3_u32 v6, v3, v2, 0
	s_movk_i32 s3, 0x7fff
	s_mov_b32 s4, 0xffff0000
	s_movk_i32 s5, 0x4000
	v_mov_b32_e32 v7, s79
	s_waitcnt vmcnt(31)
	v_mov_b32_e32 v8, s77
	s_waitcnt vmcnt(30)
	v_mov_b32_e32 v9, s78
	v_mov_b32_e32 v10, s76
	v_mov_b32_e32 v3, 0
	s_mov_b32 s6, 0
	v_add_u32_e32 v2, s2, v150
	s_cmp_lt_u32 s6, 8
	v_and_b32_e32 v11, 0x2ffc, v2
	v_add_u32_e32 v40, 0x800, v2
	v_add_u32_e32 v41, 0x1000, v2
	s_cselect_b32 s11, s77, s79
	s_cselect_b32 s10, s76, s78
	s_cmpk_lt_u32 s2, 0x4000
	v_add_u32_e32 v2, 0x1800, v2
	v_lshlrev_b32_e32 v11, 2, v11
	v_and_b32_e32 v44, 0x3ffc, v40
	v_cmp_gt_u32_e32 vcc, s5, v40
	v_and_b32_e32 v45, 0x3ffc, v41
	s_cselect_b32 s13, s77, s79
	v_cndmask_b32_e32 v49, v7, v8, vcc
	s_cselect_b32 s12, s76, s78
	v_and_b32_e32 v50, 0x3ffc, v2
	v_cmp_gt_u32_e64 s[0:1], s5, v2
	global_load_dwordx4 v[40:43], v11, s[10:11]
	v_cndmask_b32_e32 v48, v9, v10, vcc
	v_lshlrev_b32_e32 v2, 2, v44
	v_lshlrev_b32_e32 v11, 2, v45
	v_cndmask_b32_e64 v53, v7, v8, s[0:1]
	v_cndmask_b32_e64 v52, v9, v10, s[0:1]
	global_load_dwordx4 v[44:47], v11, s[12:13]
	v_lshl_add_u64 v[48:49], v[48:49], 0, v[2:3]
	v_lshlrev_b32_e32 v2, 2, v50
	global_load_dwordx4 v[48:51], v[48:49], off
	v_lshl_add_u64 v[52:53], v[52:53], 0, v[2:3]
	global_load_dwordx4 v[52:55], v[52:53], off
	s_add_i32 s6, s6, 4
	s_addk_i32 s2, 0x2000
	s_cmpk_eq_u32 s2, 0x8000
	v_add_u32_e32 v2, s2, v150
	s_cmp_lt_u32 s6, 8
	v_and_b32_e32 v11, 0x2ffc, v2
	v_add_u32_e32 v56, 0x800, v2
	v_add_u32_e32 v57, 0x1000, v2
	s_cselect_b32 s11, s77, s79
	s_cselect_b32 s10, s76, s78
	s_cmpk_lt_u32 s2, 0x4000
	v_add_u32_e32 v2, 0x1800, v2
	v_lshlrev_b32_e32 v11, 2, v11
	v_and_b32_e32 v60, 0x3ffc, v56
	v_cmp_gt_u32_e32 vcc, s5, v56
	v_and_b32_e32 v61, 0x3ffc, v57
	s_cselect_b32 s13, s77, s79
	v_cndmask_b32_e32 v65, v7, v8, vcc
	s_cselect_b32 s12, s76, s78
	v_and_b32_e32 v66, 0x3ffc, v2
	v_cmp_gt_u32_e64 s[0:1], s5, v2
	global_load_dwordx4 v[56:59], v11, s[10:11]
	v_cndmask_b32_e32 v64, v9, v10, vcc
	v_lshlrev_b32_e32 v2, 2, v60
	v_lshlrev_b32_e32 v11, 2, v61
	v_cndmask_b32_e64 v69, v7, v8, s[0:1]
	v_cndmask_b32_e64 v68, v9, v10, s[0:1]
	global_load_dwordx4 v[60:63], v11, s[12:13]
	v_lshl_add_u64 v[64:65], v[64:65], 0, v[2:3]
	v_lshlrev_b32_e32 v2, 2, v66
	global_load_dwordx4 v[64:67], v[64:65], off
	v_lshl_add_u64 v[68:69], v[68:69], 0, v[2:3]
	global_load_dwordx4 v[68:71], v[68:69], off
	s_add_i32 s6, s6, 4
	s_addk_i32 s2, 0x2000
	s_cmpk_eq_u32 s2, 0x8000
	v_add_u32_e32 v2, s2, v150
	s_cmp_lt_u32 s6, 8
	v_and_b32_e32 v11, 0x2ffc, v2
	v_add_u32_e32 v72, 0x800, v2
	v_add_u32_e32 v73, 0x1000, v2
	s_cselect_b32 s11, s77, s79
	s_cselect_b32 s10, s76, s78
	s_cmpk_lt_u32 s2, 0x4000
	v_add_u32_e32 v2, 0x1800, v2
	v_lshlrev_b32_e32 v11, 2, v11
	v_and_b32_e32 v76, 0x3ffc, v72
	v_cmp_gt_u32_e32 vcc, s5, v72
	v_and_b32_e32 v77, 0x3ffc, v73
	s_cselect_b32 s13, s77, s79
	v_cndmask_b32_e32 v81, v7, v8, vcc
	s_cselect_b32 s12, s76, s78
	v_and_b32_e32 v82, 0x3ffc, v2
	v_cmp_gt_u32_e64 s[0:1], s5, v2
	global_load_dwordx4 v[72:75], v11, s[10:11]
	v_cndmask_b32_e32 v80, v9, v10, vcc
	v_lshlrev_b32_e32 v2, 2, v76
	v_lshlrev_b32_e32 v11, 2, v77
	v_cndmask_b32_e64 v85, v7, v8, s[0:1]
	v_cndmask_b32_e64 v84, v9, v10, s[0:1]
	global_load_dwordx4 v[76:79], v11, s[12:13]
	v_lshl_add_u64 v[80:81], v[80:81], 0, v[2:3]
	v_lshlrev_b32_e32 v2, 2, v82
	global_load_dwordx4 v[80:83], v[80:81], off
	v_lshl_add_u64 v[84:85], v[84:85], 0, v[2:3]
	global_load_dwordx4 v[84:87], v[84:85], off
	s_add_i32 s6, s6, 4
	s_addk_i32 s2, 0x2000
	s_cmpk_eq_u32 s2, 0x8000
	v_add_u32_e32 v2, s2, v150
	s_cmp_lt_u32 s6, 8
	v_and_b32_e32 v11, 0x2ffc, v2
	v_add_u32_e32 v88, 0x800, v2
	v_add_u32_e32 v89, 0x1000, v2
	s_cselect_b32 s11, s77, s79
	s_cselect_b32 s10, s76, s78
	s_cmpk_lt_u32 s2, 0x4000
	v_add_u32_e32 v2, 0x1800, v2
	v_lshlrev_b32_e32 v11, 2, v11
	v_and_b32_e32 v92, 0x3ffc, v88
	v_cmp_gt_u32_e32 vcc, s5, v88
	v_and_b32_e32 v93, 0x3ffc, v89
	s_cselect_b32 s13, s77, s79
	v_cndmask_b32_e32 v97, v7, v8, vcc
	s_cselect_b32 s12, s76, s78
	v_and_b32_e32 v98, 0x3ffc, v2
	v_cmp_gt_u32_e64 s[0:1], s5, v2
	global_load_dwordx4 v[88:91], v11, s[10:11]
	v_cndmask_b32_e32 v96, v9, v10, vcc
	v_lshlrev_b32_e32 v2, 2, v92
	v_lshlrev_b32_e32 v11, 2, v93
	v_cndmask_b32_e64 v101, v7, v8, s[0:1]
	v_cndmask_b32_e64 v100, v9, v10, s[0:1]
	global_load_dwordx4 v[92:95], v11, s[12:13]
	v_lshl_add_u64 v[96:97], v[96:97], 0, v[2:3]
	v_lshlrev_b32_e32 v2, 2, v98
	global_load_dwordx4 v[96:99], v[96:97], off
	v_lshl_add_u64 v[100:101], v[100:101], 0, v[2:3]
	global_load_dwordx4 v[100:103], v[100:101], off
	s_add_i32 s6, s6, 4
	s_addk_i32 s2, 0x2000
	s_cmpk_eq_u32 s2, 0x8000
	s_waitcnt vmcnt(15)
; #define GAS __attribute__((address_space(1)))
; #define LAS __attribute__((address_space(3)))
; DI unsigned f2bf(float f) { unsigned u = __builtin_bit_cast(unsigned, f); return (u + 0x7fffu + ((u >> 16) & 1u)) >> 16; }
; DI unsigned pk2(float lo, float hi) { return f2bf(lo) | (f2bf(hi) << 16); }
; DI void p8_phase(Frame& F) {
;     ...
; #pragma unroll 4
;     for (int i = 0; i < 16; ++i) { const int idx = tid * 4 + 2048 * i, side = idx >> 14, rem = idx & 16383, row = rem >> 7, col = rem & 127;
;         const f32x4 a = *(const GAS f32x4*)((side ? F.keys2 : F.keys1) + rem);
;         v2u o; o.x = pk2(a.x, a.y); o.y = pk2(a.z, a.w); *(LAS v2u*)(KIMG + (side * 128 + row) * KPITCH + col * 2) = o; }
;     __syncthreads();
	v_bfe_u32 v2, v40, 16, 1
	v_bfe_u32 v28, v42, 16, 1
	v_bfe_u32 v11, v41, 16, 1
	v_bfe_u32 v29, v43, 16, 1
	v_add3_u32 v2, v40, v2, s3
	v_add3_u32 v40, v42, v28, s3
	s_waitcnt vmcnt(14)
	v_bfe_u32 v42, v44, 16, 1
	v_bfe_u32 v28, v46, 16, 1
	v_add3_u32 v11, v41, v11, s3
	v_add3_u32 v41, v43, v29, s3
	v_bfe_u32 v43, v45, 16, 1
	v_bfe_u32 v29, v47, 16, 1
	v_lshrrev_b32_e32 v2, 16, v2
	v_lshrrev_b32_e32 v30, 16, v40
	s_waitcnt vmcnt(13)
	v_bfe_u32 v31, v48, 16, 1
	v_bfe_u32 v33, v50, 16, 1
	v_add3_u32 v42, v44, v42, s3
	v_add3_u32 v44, v46, v28, s3
	v_bfe_u32 v32, v49, 16, 1
	v_bfe_u32 v34, v51, 16, 1
	v_add3_u32 v43, v45, v43, s3
	v_add3_u32 v45, v47, v29, s3
	v_and_or_b32 v40, v11, s4, v2
	v_and_or_b32 v41, v41, s4, v30
	v_add3_u32 v2, v48, v31, s3
	v_add3_u32 v46, v50, v33, s3
	v_lshrrev_b32_e32 v44, 16, v44
	s_waitcnt vmcnt(12)
	v_bfe_u32 v48, v52, 16, 1
	v_bfe_u32 v50, v54, 16, 1
	v_add3_u32 v11, v49, v32, s3
	v_add3_u32 v47, v51, v34, s3
	v_lshrrev_b32_e32 v42, 16, v42
	v_bfe_u32 v49, v53, 16, 1
	v_bfe_u32 v51, v55, 16, 1
	ds_write_b64 v6, v[40:41]
	v_lshrrev_b32_e32 v2, 16, v2
	v_lshrrev_b32_e32 v46, 16, v46
	v_and_or_b32 v41, v45, s4, v44
	v_add3_u32 v44, v52, v48, s3
	v_add3_u32 v48, v54, v50, s3
	v_and_or_b32 v40, v43, s4, v42
	v_add3_u32 v45, v53, v49, s3
	v_add3_u32 v49, v55, v51, s3
	v_and_or_b32 v42, v11, s4, v2
	v_and_or_b32 v43, v47, s4, v46
	v_lshrrev_b32_e32 v2, 16, v44
	v_lshrrev_b32_e32 v11, 16, v48
	ds_write_b64 v5, v[42:43]
	ds_write_b64 v4, v[40:41]
	v_and_or_b32 v40, v45, s4, v2
	v_and_or_b32 v41, v49, s4, v11
	ds_write_b64 v1, v[40:41]
	s_waitcnt vmcnt(11)
	v_bfe_u32 v2, v56, 16, 1
	v_bfe_u32 v28, v58, 16, 1
	v_bfe_u32 v11, v57, 16, 1
	v_bfe_u32 v29, v59, 16, 1
	v_add3_u32 v2, v56, v2, s3
	v_add3_u32 v56, v58, v28, s3
	s_waitcnt vmcnt(10)
	v_bfe_u32 v58, v60, 16, 1
	v_bfe_u32 v28, v62, 16, 1
	v_add3_u32 v11, v57, v11, s3
	v_add3_u32 v57, v59, v29, s3
	v_bfe_u32 v59, v61, 16, 1
	v_bfe_u32 v29, v63, 16, 1
	v_lshrrev_b32_e32 v2, 16, v2
	v_lshrrev_b32_e32 v30, 16, v56
	s_waitcnt vmcnt(9)
	v_bfe_u32 v31, v64, 16, 1
	v_bfe_u32 v33, v66, 16, 1
	v_add3_u32 v58, v60, v58, s3
	v_add3_u32 v60, v62, v28, s3
	v_bfe_u32 v32, v65, 16, 1
	v_bfe_u32 v34, v67, 16, 1
	v_add3_u32 v59, v61, v59, s3
	v_add3_u32 v61, v63, v29, s3
	v_and_or_b32 v56, v11, s4, v2
	v_and_or_b32 v57, v57, s4, v30
	v_add3_u32 v2, v64, v31, s3
	v_add3_u32 v62, v66, v33, s3
	v_lshrrev_b32_e32 v60, 16, v60
	s_waitcnt vmcnt(8)
	v_bfe_u32 v64, v68, 16, 1
	v_bfe_u32 v66, v70, 16, 1
	v_add3_u32 v11, v65, v32, s3
	v_add3_u32 v63, v67, v34, s3
	v_lshrrev_b32_e32 v58, 16, v58
	v_bfe_u32 v65, v69, 16, 1
	v_bfe_u32 v67, v71, 16, 1
	ds_write_b64 v6, v[56:57] offset:17408
	v_lshrrev_b32_e32 v2, 16, v2
	v_lshrrev_b32_e32 v62, 16, v62
	v_and_or_b32 v57, v61, s4, v60
	v_add3_u32 v60, v68, v64, s3
	v_add3_u32 v64, v70, v66, s3
	v_and_or_b32 v56, v59, s4, v58
	v_add3_u32 v61, v69, v65, s3
	v_add3_u32 v65, v71, v67, s3
	v_and_or_b32 v58, v11, s4, v2
	v_and_or_b32 v59, v63, s4, v62
	v_lshrrev_b32_e32 v2, 16, v60
	v_lshrrev_b32_e32 v11, 16, v64
	ds_write_b64 v5, v[58:59] offset:17408
	ds_write_b64 v4, v[56:57] offset:17408
	v_and_or_b32 v56, v61, s4, v2
	v_and_or_b32 v57, v65, s4, v11
	ds_write_b64 v1, v[56:57] offset:17408
	s_waitcnt vmcnt(7)
	v_bfe_u32 v2, v72, 16, 1
	v_bfe_u32 v28, v74, 16, 1
	v_bfe_u32 v11, v73, 16, 1
	v_bfe_u32 v29, v75, 16, 1
	v_add3_u32 v2, v72, v2, s3
	v_add3_u32 v72, v74, v28, s3
	s_waitcnt vmcnt(6)
	v_bfe_u32 v74, v76, 16, 1
	v_bfe_u32 v28, v78, 16, 1
	v_add3_u32 v11, v73, v11, s3
	v_add3_u32 v73, v75, v29, s3
	v_bfe_u32 v75, v77, 16, 1
	v_bfe_u32 v29, v79, 16, 1
	v_lshrrev_b32_e32 v2, 16, v2
	v_lshrrev_b32_e32 v30, 16, v72
	s_waitcnt vmcnt(5)
	v_bfe_u32 v31, v80, 16, 1
	v_bfe_u32 v33, v82, 16, 1
	v_add3_u32 v74, v76, v74, s3
	v_add3_u32 v76, v78, v28, s3
	v_bfe_u32 v32, v81, 16, 1
	v_bfe_u32 v34, v83, 16, 1
	v_add3_u32 v75, v77, v75, s3
	v_add3_u32 v77, v79, v29, s3
	v_and_or_b32 v72, v11, s4, v2
	v_and_or_b32 v73, v73, s4, v30
	v_add3_u32 v2, v80, v31, s3
	v_add3_u32 v78, v82, v33, s3
	v_lshrrev_b32_e32 v76, 16, v76
	s_waitcnt vmcnt(4)
	v_bfe_u32 v80, v84, 16, 1
	v_bfe_u32 v82, v86, 16, 1
	v_add3_u32 v11, v81, v32, s3
	v_add3_u32 v79, v83, v34, s3
	v_lshrrev_b32_e32 v74, 16, v74
	v_bfe_u32 v81, v85, 16, 1
	v_bfe_u32 v83, v87, 16, 1
	ds_write_b64 v6, v[72:73] offset:34816
	v_lshrrev_b32_e32 v2, 16, v2
	v_lshrrev_b32_e32 v78, 16, v78
	v_and_or_b32 v73, v77, s4, v76
	v_add3_u32 v76, v84, v80, s3
	v_add3_u32 v80, v86, v82, s3
	v_and_or_b32 v72, v75, s4, v74
	v_add3_u32 v77, v85, v81, s3
	v_add3_u32 v81, v87, v83, s3
	v_and_or_b32 v74, v11, s4, v2
	v_and_or_b32 v75, v79, s4, v78
	v_lshrrev_b32_e32 v2, 16, v76
	v_lshrrev_b32_e32 v11, 16, v80
	ds_write_b64 v5, v[74:75] offset:34816
	ds_write_b64 v4, v[72:73] offset:34816
	v_and_or_b32 v72, v77, s4, v2
	v_and_or_b32 v73, v81, s4, v11
	ds_write_b64 v1, v[72:73] offset:34816
	s_waitcnt vmcnt(3)
	v_bfe_u32 v2, v88, 16, 1
	v_bfe_u32 v28, v90, 16, 1
	v_bfe_u32 v11, v89, 16, 1
	v_bfe_u32 v29, v91, 16, 1
	v_add3_u32 v2, v88, v2, s3
	v_add3_u32 v88, v90, v28, s3
	s_waitcnt vmcnt(2)
	v_bfe_u32 v90, v92, 16, 1
	v_bfe_u32 v28, v94, 16, 1
	v_add3_u32 v11, v89, v11, s3
	v_add3_u32 v89, v91, v29, s3
	v_bfe_u32 v91, v93, 16, 1
	v_bfe_u32 v29, v95, 16, 1
	v_lshrrev_b32_e32 v2, 16, v2
	v_lshrrev_b32_e32 v30, 16, v88
	s_waitcnt vmcnt(1)
	v_bfe_u32 v31, v96, 16, 1
	v_bfe_u32 v33, v98, 16, 1
	v_add3_u32 v90, v92, v90, s3
	v_add3_u32 v92, v94, v28, s3
	v_bfe_u32 v32, v97, 16, 1
	v_bfe_u32 v34, v99, 16, 1
	v_add3_u32 v91, v93, v91, s3
	v_add3_u32 v93, v95, v29, s3
	v_and_or_b32 v88, v11, s4, v2
	v_and_or_b32 v89, v89, s4, v30
	v_add3_u32 v2, v96, v31, s3
	v_add3_u32 v94, v98, v33, s3
	v_lshrrev_b32_e32 v92, 16, v92
	s_waitcnt vmcnt(0)
	v_bfe_u32 v96, v100, 16, 1
	v_bfe_u32 v98, v102, 16, 1
	v_add3_u32 v11, v97, v32, s3
	v_add3_u32 v95, v99, v34, s3
	v_lshrrev_b32_e32 v90, 16, v90
	v_bfe_u32 v97, v101, 16, 1
	v_bfe_u32 v99, v103, 16, 1
	ds_write_b64 v6, v[88:89] offset:52224
	v_lshrrev_b32_e32 v2, 16, v2
	v_lshrrev_b32_e32 v94, 16, v94
	v_and_or_b32 v89, v93, s4, v92
	v_add3_u32 v92, v100, v96, s3
	v_add3_u32 v96, v102, v98, s3
	v_and_or_b32 v88, v91, s4, v90
	v_add3_u32 v93, v101, v97, s3
	v_add3_u32 v97, v103, v99, s3
	v_and_or_b32 v90, v11, s4, v2
	v_and_or_b32 v91, v95, s4, v94
	v_lshrrev_b32_e32 v2, 16, v92
	v_lshrrev_b32_e32 v11, 16, v96
	ds_write_b64 v5, v[90:91] offset:52224
	ds_write_b64 v4, v[88:89] offset:52224
	v_and_or_b32 v88, v93, s4, v2
	v_and_or_b32 v89, v97, s4, v11
	ds_write_b64 v1, v[88:89] offset:52224
	v_add_u32_e32 v6, 0x11000, v6
	v_add_u32_e32 v4, 0x11000, v4
	v_add_u32_e32 v5, 0x11000, v5
	v_add_u32_e32 v1, 0x11000, v1
	v_readlane_b32 s0, v252, 12
	s_lshl_b32 s35, s0, 3
	v_readlane_b32 s0, v252, 11
	s_lshl_b32 s34, s0, 3
	s_andn2_b64 vcc, exec, s[22:23]
	s_mov_b32 s10, 0
	s_waitcnt lgkmcnt(0)
	s_barrier
; #define GAS __attribute__((address_space(1)))
; #define LAS __attribute__((address_space(3)))
; DI unsigned pk2(float lo, float hi) { return f2bf(lo) | (f2bf(hi) << 16); }
; DI int crow(int reg, int h) { return (reg & 3) + 8 * (reg >> 2) + 4 * h; }
; DI void p8_phase(Frame& F) {
;     LAS unsigned char* KIMG = F.lds; LAS unsigned char* TBL = F.lds + P8_TBL + F.wave * 1024;
;     const int lane = F.lane, tid = F.tid, r = lane & 31, h = lane >> 5;
; #pragma unroll 4
;     for (int i = 0; i < 16; ++i) { const int idx = tid * 4 + 2048 * i, side = idx >> 14, rem = idx & 16383, row = rem >> 7, col = rem & 127;
;         const f32x4 a = *(const GAS f32x4*)((side ? F.keys2 : F.keys1) + rem);
;         v2u o; o.x = pk2(a.x, a.y); o.y = pk2(a.z, a.w); *(LAS v2u*)(KIMG + (side * 128 + row) * KPITCH + col * 2) = o; }
;     __syncthreads();
;     const int gcT = F.vcu * NWAVES + F.wave, NGWT = F.G * NWAVES; int trow_it = 0;
;     for (int it = (int)blockIdx.x; it < (M / 256) * PH; it += F.G, ++trow_it) {
;         const int tile = it / PH, hd = it % PH;
;         const int t = tile * 256 + F.wave * 32 + r;
;     ...
;                 for (int reg = 0; reg < 16; ++reg) { const unsigned key = (unsigned)(kt * 32 + crow(reg, h)); const float sv = acc[kt][reg];
	s_cbranch_vccnz .LBB0_1237
	v_mbcnt_hi_u32_b32 v1, -1, v200
	v_and_b32_e32 v3, 64, v1
	v_xor_b32_e32 v2, 32, v1
	v_add_u32_e32 v3, 64, v3
	s_lshl_b32 s0, s89, 10
	v_cmp_lt_i32_e32 vcc, v2, v3
	s_add_i32 s0, s0, 0
	s_add_i32 s2, s0, 0x11000
	v_cndmask_b32_e32 v1, v1, v2, vcc
	v_lshlrev_b32_e32 v130, 3, v197
	v_lshlrev_b32_e32 v131, 2, v197
	v_lshlrev_b32_e32 v137, 2, v1
	v_lshlrev_b32_e32 v1, 5, v148
	s_add_i32 s36, s35, s89
	s_mov_b32 s11, 0
	v_mov_b32_e32 v133, 0
	v_cmp_gt_u32_e64 s[0:1], 32, v148
	v_cmp_lt_u32_e64 s[6:7], 31, v148
	v_lshl_add_u32 v139, v149, 5, s2
	v_lshl_add_u32 v144, v197, 4, 0
	v_lshl_or_b32 v145, s89, 5, v149
	v_cmp_eq_u32_e64 s[4:5], 0, v148
	s_movk_i32 s38, 0xff00
	v_lshlrev_b32_e32 v134, 1, v130
	s_movk_i32 s40, 0x110
	s_movk_i32 s41, 0x1000
	s_mov_b32 s42, 0x42fe0000
	s_mov_b32 s43, 0x40c0c00
	s_movk_i32 s44, 0xff80
	s_mov_b32 s45, 0xff61b1e6
	v_add_u32_e32 v215, s2, v1
	s_mov_b32 s46, 0
	s_mov_b32 s47, s58
	s_branch .LBB0_1207

; #define GAS __attribute__((address_space(1)))
; #define LAS __attribute__((address_space(3)))
; #define MFMA32(a, b, c) __builtin_amdgcn_mfma_f32_32x32x16_bf16((a), (b), (c), 0, 0, 0)
; DI void trow_load(Frame& F, int row, f32x4 (&v)[8]) {
;     if (row < 2 * NEXP) { const int tb = row >= NEXP, e = row - tb * NEXP; const GAS f32x4* src = (const GAS f32x4*)((tb ? F.e_up : F.e_down) + (size_t)e * D) + F.lane;
; #pragma unroll
;         for (int j = 0; j < 8; ++j) v[j] = __builtin_nontemporal_load(src + 64 * j); }
;     else {
; #pragma unroll
;         for (int j = 0; j < 8; ++j) v[j] = (f32x4){0.f, 0.f, 0.f, 0.f}; }
; }
; DI void p8_phase(Frame& F) {
;     ...
;             const bf16* qp = F.QB + (size_t)t * D + hd * 256 + side * 128 + 8 * h;
; #pragma unroll
;             for (int ks = 0; ks < 8; ++ks) {
;                 const bf16x8 qf = __builtin_nontemporal_load((const GAS bf16x8*)(qp + ks * 16));
; #pragma unroll
;                 for (int kt = 0; kt < 4; ++kt) { const bf16x8 kf = *(const LAS bf16x8*)(KIMG + (side * 128 + kt * 32 + r) * KPITCH + (ks * 16 + 8 * h) * 2); acc[kt] = MFMA32(kf, qf, acc[kt]); }
;             }
;             trow_load(F, q0 * NGWT + gcT, ra); trow_load(F, (q0 + 1) * NGWT + gcT, rb);
.LBB0_1208:
	s_lshl_b32 s10, s22, 8
	v_lshl_add_u64 v[94:95], v[142:143], 0, s[10:11]
	global_load_dwordx4 v[66:69], v[94:95], off nt
	global_load_dwordx4 v[70:73], v[94:95], off offset:32 nt
	global_load_dwordx4 v[74:77], v[94:95], off offset:64 nt
	global_load_dwordx4 v[78:81], v[94:95], off offset:96 nt
	global_load_dwordx4 v[82:85], v[94:95], off offset:128 nt
	global_load_dwordx4 v[86:89], v[94:95], off offset:160 nt
	global_load_dwordx4 v[90:93], v[94:95], off offset:192 nt
	global_load_dwordx4 v[100:103], v[94:95], off offset:224 nt
	v_lshl_or_b32 v6, s22, 7, v149
	v_mad_u32_u24 v98, v6, s40, v144
	s_lshl_b32 s10, s22, 2
	s_or_b32 s10, s10, s49
	s_mul_i32 s10, s10, s34
	s_add_i32 s10, s10, s36
	v_lshlrev_b32_e32 v132, 4, v148
	ds_read_b128 v[104:107], v98
	ds_read_b128 v[108:111], v98 offset:8704
	ds_read_b128 v[112:115], v98 offset:17408
	ds_read_b128 v[116:119], v98 offset:26112
	s_waitcnt vmcnt(7) lgkmcnt(3)
	v_mfma_f32_32x32x16_bf16 v[50:65], v[104:107], v[66:69], 0
	s_waitcnt lgkmcnt(2)
	v_mfma_f32_32x32x16_bf16 v[34:49], v[108:111], v[66:69], 0
	s_waitcnt lgkmcnt(1)
	v_mfma_f32_32x32x16_bf16 v[18:33], v[112:115], v[66:69], 0
	s_waitcnt lgkmcnt(0)
	v_mfma_f32_32x32x16_bf16 v[2:17], v[116:119], v[66:69], 0
	ds_read_b128 v[104:107], v98 offset:32
	ds_read_b128 v[108:111], v98 offset:8736
	ds_read_b128 v[112:115], v98 offset:17440
	ds_read_b128 v[116:119], v98 offset:26144
	s_waitcnt vmcnt(6) lgkmcnt(3)
	v_mfma_f32_32x32x16_bf16 v[50:65], v[104:107], v[70:73], v[50:65]
	s_waitcnt lgkmcnt(2)
	v_mfma_f32_32x32x16_bf16 v[34:49], v[108:111], v[70:73], v[34:49]
	s_waitcnt lgkmcnt(1)
	v_mfma_f32_32x32x16_bf16 v[18:33], v[112:115], v[70:73], v[18:33]
	s_waitcnt lgkmcnt(0)
	v_mfma_f32_32x32x16_bf16 v[2:17], v[116:119], v[70:73], v[2:17]
	ds_read_b128 v[104:107], v98 offset:64
	ds_read_b128 v[108:111], v98 offset:8768
	ds_read_b128 v[112:115], v98 offset:17472
	ds_read_b128 v[116:119], v98 offset:26176
	s_waitcnt vmcnt(5) lgkmcnt(3)
	v_mfma_f32_32x32x16_bf16 v[50:65], v[104:107], v[74:77], v[50:65]
	s_waitcnt lgkmcnt(2)
	v_mfma_f32_32x32x16_bf16 v[34:49], v[108:111], v[74:77], v[34:49]
	s_waitcnt lgkmcnt(1)
	v_mfma_f32_32x32x16_bf16 v[18:33], v[112:115], v[74:77], v[18:33]
	s_waitcnt lgkmcnt(0)
	v_mfma_f32_32x32x16_bf16 v[2:17], v[116:119], v[74:77], v[2:17]
	ds_read_b128 v[104:107], v98 offset:96
	ds_read_b128 v[108:111], v98 offset:8800
	ds_read_b128 v[112:115], v98 offset:17504
	ds_read_b128 v[116:119], v98 offset:26208
	s_waitcnt vmcnt(4) lgkmcnt(3)
	v_mfma_f32_32x32x16_bf16 v[50:65], v[104:107], v[78:81], v[50:65]
	s_waitcnt lgkmcnt(2)
	v_mfma_f32_32x32x16_bf16 v[34:49], v[108:111], v[78:81], v[34:49]
	s_waitcnt lgkmcnt(1)
	v_mfma_f32_32x32x16_bf16 v[18:33], v[112:115], v[78:81], v[18:33]
	s_waitcnt lgkmcnt(0)
	v_mfma_f32_32x32x16_bf16 v[2:17], v[116:119], v[78:81], v[2:17]
	ds_read_b128 v[104:107], v98 offset:128
	ds_read_b128 v[108:111], v98 offset:8832
	ds_read_b128 v[112:115], v98 offset:17536
	ds_read_b128 v[116:119], v98 offset:26240
	s_waitcnt vmcnt(3) lgkmcnt(3)
	v_mfma_f32_32x32x16_bf16 v[50:65], v[104:107], v[82:85], v[50:65]
	s_waitcnt lgkmcnt(2)
	v_mfma_f32_32x32x16_bf16 v[34:49], v[108:111], v[82:85], v[34:49]
	s_waitcnt lgkmcnt(1)
	v_mfma_f32_32x32x16_bf16 v[18:33], v[112:115], v[82:85], v[18:33]
	s_waitcnt lgkmcnt(0)
	v_mfma_f32_32x32x16_bf16 v[2:17], v[116:119], v[82:85], v[2:17]
	ds_read_b128 v[104:107], v98 offset:160
	ds_read_b128 v[108:111], v98 offset:8864
	ds_read_b128 v[112:115], v98 offset:17568
	ds_read_b128 v[116:119], v98 offset:26272
	s_waitcnt vmcnt(2) lgkmcnt(3)
	v_mfma_f32_32x32x16_bf16 v[50:65], v[104:107], v[86:89], v[50:65]
	s_waitcnt lgkmcnt(2)
	v_mfma_f32_32x32x16_bf16 v[34:49], v[108:111], v[86:89], v[34:49]
	s_waitcnt lgkmcnt(1)
	v_mfma_f32_32x32x16_bf16 v[18:33], v[112:115], v[86:89], v[18:33]
	s_waitcnt lgkmcnt(0)
	v_mfma_f32_32x32x16_bf16 v[2:17], v[116:119], v[86:89], v[2:17]
	ds_read_b128 v[104:107], v98 offset:192
	ds_read_b128 v[108:111], v98 offset:8896
	ds_read_b128 v[112:115], v98 offset:17600
	ds_read_b128 v[116:119], v98 offset:26304
	s_waitcnt vmcnt(1) lgkmcnt(3)
	v_mfma_f32_32x32x16_bf16 v[50:65], v[104:107], v[90:93], v[50:65]
	s_waitcnt lgkmcnt(2)
	v_mfma_f32_32x32x16_bf16 v[34:49], v[108:111], v[90:93], v[34:49]
	s_waitcnt lgkmcnt(1)
	v_mfma_f32_32x32x16_bf16 v[18:33], v[112:115], v[90:93], v[18:33]
	s_waitcnt lgkmcnt(0)
	v_mfma_f32_32x32x16_bf16 v[2:17], v[116:119], v[90:93], v[2:17]
	ds_read_b128 v[104:107], v98 offset:224
	ds_read_b128 v[108:111], v98 offset:8928
	ds_read_b128 v[112:115], v98 offset:17632
	ds_read_b128 v[116:119], v98 offset:26336
	s_waitcnt vmcnt(0) lgkmcnt(3)
	v_mfma_f32_32x32x16_bf16 v[50:65], v[104:107], v[100:103], v[50:65]
	s_waitcnt lgkmcnt(2)
	v_mfma_f32_32x32x16_bf16 v[34:49], v[108:111], v[100:103], v[34:49]
	s_waitcnt lgkmcnt(1)
	v_mfma_f32_32x32x16_bf16 v[18:33], v[112:115], v[100:103], v[18:33]
	s_waitcnt lgkmcnt(0)
	v_mfma_f32_32x32x16_bf16 v[2:17], v[116:119], v[100:103], v[2:17]
	v_mov_b32_e32 v248, 0
	v_mov_b32_e32 v249, 0
	v_mov_b32_e32 v250, 0
	v_mov_b32_e32 v251, 0
	v_mov_b32_e32 v244, 0
	v_mov_b32_e32 v245, 0
	v_mov_b32_e32 v246, 0
	v_mov_b32_e32 v247, 0
	v_mov_b32_e32 v206, 0
	v_mov_b32_e32 v207, 0
	v_mov_b32_e32 v208, 0
	v_mov_b32_e32 v209, 0
	v_mov_b32_e32 v192, 0
	v_mov_b32_e32 v193, 0
	v_mov_b32_e32 v194, 0
	v_mov_b32_e32 v195, 0
	v_mov_b32_e32 v184, 0
	v_mov_b32_e32 v185, 0
	v_mov_b32_e32 v186, 0
	v_mov_b32_e32 v187, 0
	v_mov_b32_e32 v176, 0
	v_mov_b32_e32 v177, 0
	v_mov_b32_e32 v178, 0
	v_mov_b32_e32 v179, 0
	v_mov_b32_e32 v164, 0
	v_mov_b32_e32 v165, 0
	v_mov_b32_e32 v166, 0
	v_mov_b32_e32 v167, 0
	v_mov_b32_e32 v172, 0
	v_mov_b32_e32 v173, 0
	v_mov_b32_e32 v174, 0
	v_mov_b32_e32 v175, 0
	v_mov_b32_e32 v152, 0
	s_cmpk_gt_i32 s10, 0x7fff
	s_cbranch_scc1 .LBB0_1210
	s_cmpk_gt_i32 s10, 0x3fff
	s_cselect_b32 s12, 0xffffc000, 0
	s_cselect_b32 s22, s82, s80
	s_cselect_b32 s23, s83, s81
	s_add_i32 s12, s12, s10
	s_ashr_i32 s13, s12, 31
	s_lshl_b64 s[12:13], s[12:13], 13
	s_add_u32 s12, s22, s12
	s_addc_u32 s13, s23, s13
	v_lshl_add_u64 v[154:155], s[12:13], 0, v[132:133]
	v_add_co_u32_e32 v154, vcc, s41, v154
	global_load_dwordx4 v[248:251], v132, s[12:13] nt
	global_load_dwordx4 v[244:247], v132, s[12:13] offset:1024 nt
	global_load_dwordx4 v[206:209], v132, s[12:13] offset:2048 nt
	global_load_dwordx4 v[192:195], v132, s[12:13] offset:3072 nt
	v_addc_co_u32_e32 v155, vcc, 0, v155, vcc
	global_load_dwordx4 v[184:187], v[154:155], off nt
	global_load_dwordx4 v[176:179], v[154:155], off offset:1024 nt
	global_load_dwordx4 v[164:167], v[154:155], off offset:2048 nt
	global_load_dwordx4 v[172:175], v[154:155], off offset:3072 nt
; #define GAS __attribute__((address_space(1)))
; DI float lane_bcast(float v, int l) { return __uint_as_float((unsigned)__builtin_amdgcn_readlane((int)__float_as_uint(v), l)); }
; DI void trow_load(Frame& F, int row, f32x4 (&v)[8]) {
;     if (row < 2 * NEXP) { const int tb = row >= NEXP, e = row - tb * NEXP; const GAS f32x4* src = (const GAS f32x4*)((tb ? F.e_up : F.e_down) + (size_t)e * D) + F.lane;
; #pragma unroll
;         for (int j = 0; j < 8; ++j) v[j] = __builtin_nontemporal_load(src + 64 * j); }
;     else {
; #pragma unroll
;         for (int j = 0; j < 8; ++j) v[j] = (f32x4){0.f, 0.f, 0.f, 0.f}; }
; }
; DI void trow_store(Frame& F, int row, const f32x4 (&v)[8], float am) {
;     if (row >= 2 * NEXP) return;
;     const int tb = row >= NEXP, e = row - tb * NEXP; am = fmaxf(am, 1e-30f);
;     const float sc = am * (1.0f / 127.0f), inv = 127.0f / am;
;     GAS unsigned* dst = (GAS unsigned*)((tb ? F.EU : F.ED) + (size_t)e * D) + F.lane;
;     const int off = 0;
; #pragma unroll
;     for (int j = 0; j < 8; ++j) {
;         const int q0 = (int)__builtin_rintf(v[j].x * inv) + off, q1 = (int)__builtin_rintf(v[j].y * inv) + off, q2 = (int)__builtin_rintf(v[j].z * inv) + off, q3 = (int)__builtin_rintf(v[j].w * inv) + off;
;         dst[64 * j] = (unsigned)(q0 & 255) | ((unsigned)(q1 & 255) << 8) | ((unsigned)(q2 & 255) << 16) | ((unsigned)(q3 & 255) << 24);
;     }
;     if (F.lane == 0) (tb ? F.SU : F.SD)[e] = sc;
; }
; #pragma unroll
;     for (int j = 0; j < 8; ++j) am = fmaxf(am, fmaxf(fmaxf(fabsf(v[j].x), fabsf(v[j].y)), fmaxf(fabsf(v[j].z), fabsf(v[j].w))));
;     return am; }
; DI void trow_finish2(Frame& F, int rowA, int rowB, const f32x4 (&a)[8], const f32x4 (&b)[8]) {
;     const float m = red2_max(trow_absmax(a), trow_absmax(b));
;     trow_store(F, rowA, a, lane_bcast(m, 0)); trow_store(F, rowB, b, lane_bcast(m, 32));
; DI void p8_phase(Frame& F) {
;     ...
;             trow_load(F, q0 * NGWT + gcT, ra); trow_load(F, (q0 + 1) * NGWT + gcT, rb);
;             float L[16];
; #pragma unroll
;             for (int i = 0; i < 16; ++i) L[i] = -3.0e38f;
; #pragma unroll
;             for (int kt = 0; kt < 4; ++kt) {
;                 if (kt == 2) { trow_finish2(F, q0 * NGWT + gcT, (q0 + 1) * NGWT + gcT, ra, rb); trow_load(F, (q0 + 2) * NGWT + gcT, ra); trow_load(F, (q0 + 3) * NGWT + gcT, rb); }
.LBB0_1210:
	s_add_i32 s30, s10, s34
	s_cmpk_gt_i32 s30, 0x7fff
	v_mov_b32_e32 v153, 0
	v_mov_b32_e32 v154, 0
	v_mov_b32_e32 v155, 0
	v_mov_b32_e32 v160, 0
	v_mov_b32_e32 v161, 0
	v_mov_b32_e32 v162, 0
	v_mov_b32_e32 v163, 0
	v_mov_b32_e32 v168, 0
	v_mov_b32_e32 v169, 0
	v_mov_b32_e32 v170, 0
	v_mov_b32_e32 v171, 0
	v_mov_b32_e32 v180, 0
	v_mov_b32_e32 v181, 0
	v_mov_b32_e32 v182, 0
	v_mov_b32_e32 v183, 0
	v_mov_b32_e32 v188, 0
	v_mov_b32_e32 v189, 0
	v_mov_b32_e32 v190, 0
	v_mov_b32_e32 v191, 0
	v_mov_b32_e32 v202, 0
	v_mov_b32_e32 v203, 0
	v_mov_b32_e32 v204, 0
	v_mov_b32_e32 v205, 0
	v_mov_b32_e32 v210, 0
	v_mov_b32_e32 v211, 0
	v_mov_b32_e32 v212, 0
	v_mov_b32_e32 v213, 0
	v_mov_b32_e32 v156, 0
	v_mov_b32_e32 v157, 0
	v_mov_b32_e32 v158, 0
	v_mov_b32_e32 v159, 0
	s_cbranch_scc1 .LP7_issue_b
	s_cmpk_gt_i32 s30, 0x3fff
	s_cselect_b32 s12, 0xffffc000, 0
	s_cselect_b32 s22, s82, s80
	s_cselect_b32 s23, s83, s81
	s_add_i32 s12, s12, s30
	s_ashr_i32 s13, s12, 31
	s_lshl_b64 s[12:13], s[12:13], 13
	s_add_u32 s12, s22, s12
	s_addc_u32 s13, s23, s13
	v_lshl_add_u64 v[152:153], s[12:13], 0, v[132:133]
	v_add_co_u32_e32 v156, vcc, s41, v152
	global_load_dwordx4 v[210:213], v132, s[12:13] nt
	global_load_dwordx4 v[202:205], v132, s[12:13] offset:1024 nt
	global_load_dwordx4 v[188:191], v132, s[12:13] offset:2048 nt
	global_load_dwordx4 v[180:183], v132, s[12:13] offset:3072 nt
	v_addc_co_u32_e32 v157, vcc, 0, v153, vcc
	global_load_dwordx4 v[168:171], v[156:157], off nt
	global_load_dwordx4 v[160:163], v[156:157], off offset:1024 nt
	global_load_dwordx4 v[152:155], v[156:157], off offset:2048 nt
	s_nop 0
	global_load_dwordx4 v[156:159], v[156:157], off offset:3072 nt
.LP7_issue_b:
	s_mov_b32 s90, s10
	s_mov_b32 s91, s30

; DI int crow(int reg, int h) { return (reg & 3) + 8 * (reg >> 2) + 4 * h; }
; DI void topk_insert(float (&L)[16], float x) {
; #pragma unroll
;     for (int i = 15; i >= 1; --i) L[i] = __builtin_amdgcn_fmed3f(x, L[i - 1], L[i]);
;     L[0] = fmaxf(L[0], x);
; }
; DI void p8_phase(Frame& F) {
;     ...
;             for (int kt = 0; kt < 4; ++kt) {
;                 if (kt == 2) { trow_finish2(F, q0 * NGWT + gcT, (q0 + 1) * NGWT + gcT, ra, rb); trow_load(F, (q0 + 2) * NGWT + gcT, ra); trow_load(F, (q0 + 3) * NGWT + gcT, rb); }
; #pragma unroll
;                 for (int reg = 0; reg < 16; ++reg) { const unsigned key = (unsigned)(kt * 32 + crow(reg, h)); const float sv = acc[kt][reg];
;                     topk_insert(L, __uint_as_float((__float_as_uint(sv) & ~127u) | key)); }
.LBB0_1224:
	v_and_or_b32 v50, v50, s44, 0
	v_max_f32_e32 v132, v50, v50
	v_and_or_b32 v51, v51, s44, 1
	v_max_f32_e32 v132, 0xff61b1e6, v132
	v_max_f32_e32 v229, v51, v51
	v_and_or_b32 v52, v52, s44, 2
	v_med3_f32 v50, v50, s45, s45
	v_max_f32_e32 v229, v132, v229
	v_max_f32_e32 v230, v52, v52
	v_and_or_b32 v53, v53, s44, 3
	v_med3_f32 v132, v51, v132, v50
	v_med3_f32 v50, v51, v50, v50
	v_max_f32_e32 v230, v229, v230
	v_max_f32_e32 v231, v53, v53
	v_and_or_b32 v54, v54, s44, 4
	v_med3_f32 v229, v52, v229, v132
	v_med3_f32 v51, v52, v132, v50
	v_med3_f32 v50, v52, v50, v50
	v_max_f32_e32 v231, v230, v231
	v_max_f32_e32 v232, v54, v54
	v_and_or_b32 v55, v55, s44, 5
	v_med3_f32 v230, v53, v230, v229
	v_med3_f32 v132, v53, v229, v51
	v_med3_f32 v51, v53, v51, v50
	v_med3_f32 v50, v53, v50, v50
	v_max_f32_e32 v232, v231, v232
	v_max_f32_e32 v233, v55, v55
	v_and_or_b32 v56, v56, s44, 6
	v_med3_f32 v231, v54, v231, v230
	v_med3_f32 v229, v54, v230, v132
	v_med3_f32 v52, v54, v132, v51
	v_med3_f32 v51, v54, v51, v50
	v_med3_f32 v50, v54, v50, v50
	v_max_f32_e32 v233, v232, v233
	v_max_f32_e32 v234, v56, v56
	v_and_or_b32 v57, v57, s44, 7
	v_med3_f32 v232, v55, v232, v231
	v_med3_f32 v230, v55, v231, v229
	v_med3_f32 v132, v55, v229, v52
	v_med3_f32 v52, v55, v52, v51
	v_med3_f32 v51, v55, v51, v50
	v_med3_f32 v50, v55, v50, v50
	v_max_f32_e32 v234, v233, v234
	v_max_f32_e32 v235, v57, v57
	v_and_or_b32 v58, v58, s44, 8
	v_med3_f32 v233, v56, v233, v232
	v_med3_f32 v231, v56, v232, v230
	v_med3_f32 v229, v56, v230, v132
	v_med3_f32 v53, v56, v132, v52
	v_med3_f32 v52, v56, v52, v51
	v_med3_f32 v51, v56, v51, v50
	v_med3_f32 v50, v56, v50, v50
	v_max_f32_e32 v235, v234, v235
	v_max_f32_e32 v236, v58, v58
	v_and_or_b32 v59, v59, s44, 9
	v_med3_f32 v234, v57, v234, v233
	v_med3_f32 v232, v57, v233, v231
	v_med3_f32 v230, v57, v231, v229
	v_med3_f32 v132, v57, v229, v53
	v_med3_f32 v53, v57, v53, v52
	v_med3_f32 v52, v57, v52, v51
	v_med3_f32 v51, v57, v51, v50
	v_med3_f32 v50, v57, v50, v50
	v_max_f32_e32 v236, v235, v236
	v_max_f32_e32 v237, v59, v59
	v_and_or_b32 v60, v60, s44, 10
	v_med3_f32 v235, v58, v235, v234
	v_med3_f32 v233, v58, v234, v232
	v_med3_f32 v231, v58, v232, v230
	v_med3_f32 v229, v58, v230, v132
	v_med3_f32 v54, v58, v132, v53
	v_med3_f32 v53, v58, v53, v52
	v_med3_f32 v52, v58, v52, v51
	v_med3_f32 v51, v58, v51, v50
	v_med3_f32 v50, v58, v50, v50
	v_max_f32_e32 v237, v236, v237
	v_max_f32_e32 v238, v60, v60
	v_and_or_b32 v61, v61, s44, 11
	v_med3_f32 v236, v59, v236, v235
	v_med3_f32 v234, v59, v235, v233
	v_med3_f32 v232, v59, v233, v231
	v_med3_f32 v230, v59, v231, v229
	v_med3_f32 v132, v59, v229, v54
	v_med3_f32 v54, v59, v54, v53
	v_med3_f32 v53, v59, v53, v52
	v_med3_f32 v52, v59, v52, v51
	v_med3_f32 v51, v59, v51, v50
	v_med3_f32 v50, v59, v50, v50
	v_max_f32_e32 v238, v237, v238
	v_max_f32_e32 v239, v61, v61
	v_and_or_b32 v62, v62, s44, 12
	v_med3_f32 v237, v60, v237, v236
	v_med3_f32 v235, v60, v236, v234
	v_med3_f32 v233, v60, v234, v232
	v_med3_f32 v231, v60, v232, v230
	v_med3_f32 v229, v60, v230, v132
	v_med3_f32 v55, v60, v132, v54
	v_med3_f32 v54, v60, v54, v53
	v_med3_f32 v53, v60, v53, v52
	v_med3_f32 v52, v60, v52, v51
	v_med3_f32 v51, v60, v51, v50
	v_med3_f32 v50, v60, v50, v50
	v_max_f32_e32 v239, v238, v239
	v_max_f32_e32 v240, v62, v62
	v_and_or_b32 v63, v63, s44, 13
	v_med3_f32 v238, v61, v238, v237
	v_med3_f32 v236, v61, v237, v235
	v_med3_f32 v234, v61, v235, v233
	v_med3_f32 v232, v61, v233, v231
	v_med3_f32 v230, v61, v231, v229
	v_med3_f32 v132, v61, v229, v55
	v_med3_f32 v55, v61, v55, v54
	v_med3_f32 v54, v61, v54, v53
	v_med3_f32 v53, v61, v53, v52
	v_med3_f32 v52, v61, v52, v51
	v_med3_f32 v51, v61, v51, v50
	v_med3_f32 v50, v61, v50, v50
	v_max_f32_e32 v240, v239, v240
	v_max_f32_e32 v241, v63, v63
	v_and_or_b32 v64, v64, s44, 14
	v_med3_f32 v239, v62, v239, v238
	v_med3_f32 v237, v62, v238, v236
	v_med3_f32 v235, v62, v236, v234
	v_med3_f32 v233, v62, v234, v232
	v_med3_f32 v231, v62, v232, v230
	v_med3_f32 v229, v62, v230, v132
	v_med3_f32 v56, v62, v132, v55
	v_med3_f32 v55, v62, v55, v54
	v_med3_f32 v54, v62, v54, v53
	v_med3_f32 v53, v62, v53, v52
	v_med3_f32 v52, v62, v52, v51
	v_med3_f32 v51, v62, v51, v50
	v_med3_f32 v50, v62, v50, v50
	v_max_f32_e32 v241, v240, v241
	v_max_f32_e32 v242, v64, v64
	v_and_or_b32 v65, v65, s44, 15
	v_med3_f32 v240, v63, v240, v239
	v_med3_f32 v238, v63, v239, v237
	v_med3_f32 v236, v63, v237, v235
	v_med3_f32 v234, v63, v235, v233
	v_med3_f32 v232, v63, v233, v231
	v_med3_f32 v230, v63, v231, v229
	v_med3_f32 v132, v63, v229, v56
	v_med3_f32 v56, v63, v56, v55
	v_med3_f32 v55, v63, v55, v54
	v_med3_f32 v54, v63, v54, v53
	v_med3_f32 v53, v63, v53, v52
	v_med3_f32 v52, v63, v52, v51
	v_med3_f32 v51, v63, v51, v50
	v_med3_f32 v50, v63, v50, v50
	v_max_f32_e32 v242, v241, v242
	v_max_f32_e32 v243, v65, v65
	v_med3_f32 v241, v64, v241, v240
	v_med3_f32 v239, v64, v240, v238
	v_med3_f32 v237, v64, v238, v236
	v_med3_f32 v235, v64, v236, v234
	v_med3_f32 v233, v64, v234, v232
	v_med3_f32 v231, v64, v232, v230
	v_med3_f32 v229, v64, v230, v132
	v_med3_f32 v57, v64, v132, v56
	v_med3_f32 v56, v64, v56, v55
	v_med3_f32 v55, v64, v55, v54
	v_med3_f32 v54, v64, v54, v53
	v_med3_f32 v53, v64, v53, v52
	v_med3_f32 v52, v64, v52, v51
	v_med3_f32 v51, v64, v51, v50
	v_med3_f32 v50, v64, v50, v50
	v_max_f32_e32 v243, v242, v243
	v_med3_f32 v242, v65, v242, v241
	v_med3_f32 v240, v65, v241, v239
	v_med3_f32 v238, v65, v239, v237
	v_med3_f32 v236, v65, v237, v235
	v_med3_f32 v234, v65, v235, v233
	v_med3_f32 v232, v65, v233, v231
	v_med3_f32 v230, v65, v231, v229
; DI int crow(int reg, int h) { return (reg & 3) + 8 * (reg >> 2) + 4 * h; }
; DI void topk_insert(float (&L)[16], float x) {
; #pragma unroll
;     for (int i = 15; i >= 1; --i) L[i] = __builtin_amdgcn_fmed3f(x, L[i - 1], L[i]);
;     L[0] = fmaxf(L[0], x);
; }
; DI void p8_phase(Frame& F) {
;     ...
;             for (int kt = 0; kt < 4; ++kt) {
;                 if (kt == 2) { trow_finish2(F, q0 * NGWT + gcT, (q0 + 1) * NGWT + gcT, ra, rb); trow_load(F, (q0 + 2) * NGWT + gcT, ra); trow_load(F, (q0 + 3) * NGWT + gcT, rb); }
; #pragma unroll
;                 for (int reg = 0; reg < 16; ++reg) { const unsigned key = (unsigned)(kt * 32 + crow(reg, h)); const float sv = acc[kt][reg];
;                     topk_insert(L, __uint_as_float((__float_as_uint(sv) & ~127u) | key)); }
	v_med3_f32 v132, v65, v229, v57
	v_med3_f32 v57, v65, v57, v56
	v_med3_f32 v56, v65, v56, v55
	v_med3_f32 v55, v65, v55, v54
	v_med3_f32 v54, v65, v54, v53
	v_med3_f32 v53, v65, v53, v52
	v_med3_f32 v52, v65, v52, v51
	v_med3_f32 v50, v65, v51, v50
	v_and_or_b32 v34, v34, s44, 16
	v_med3_f32 v50, v34, v52, v50
	v_med3_f32 v51, v34, v53, v52
	v_med3_f32 v52, v34, v54, v53
	v_med3_f32 v53, v34, v55, v54
	v_med3_f32 v54, v34, v56, v55
	v_med3_f32 v55, v34, v57, v56
	v_med3_f32 v56, v34, v132, v57
	v_med3_f32 v57, v34, v230, v132
	v_med3_f32 v58, v34, v232, v230
	v_med3_f32 v59, v34, v234, v232
	v_med3_f32 v60, v34, v236, v234
	v_med3_f32 v61, v34, v238, v236
	v_med3_f32 v62, v34, v240, v238
	v_med3_f32 v63, v34, v242, v240
	v_med3_f32 v64, v34, v243, v242
	v_max_f32_e32 v34, v34, v34
	v_max_f32_e32 v34, v243, v34
	v_and_or_b32 v35, v35, s44, 17
	v_med3_f32 v50, v35, v51, v50
	v_med3_f32 v51, v35, v52, v51
	v_med3_f32 v52, v35, v53, v52
	v_med3_f32 v53, v35, v54, v53
	v_med3_f32 v54, v35, v55, v54
	v_med3_f32 v55, v35, v56, v55
	v_med3_f32 v56, v35, v57, v56
	v_med3_f32 v57, v35, v58, v57
	v_med3_f32 v58, v35, v59, v58
	v_med3_f32 v59, v35, v60, v59
	v_med3_f32 v60, v35, v61, v60
	v_med3_f32 v61, v35, v62, v61
	v_med3_f32 v62, v35, v63, v62
	v_med3_f32 v63, v35, v64, v63
	v_med3_f32 v64, v35, v34, v64
	v_max_f32_e32 v35, v35, v35
	v_max_f32_e32 v34, v34, v35
	v_and_or_b32 v35, v36, s44, 18
	v_med3_f32 v36, v35, v51, v50
	v_med3_f32 v50, v35, v52, v51
	v_med3_f32 v51, v35, v53, v52
	v_med3_f32 v52, v35, v54, v53
	v_med3_f32 v53, v35, v55, v54
	v_med3_f32 v54, v35, v56, v55
	v_med3_f32 v55, v35, v57, v56
	v_med3_f32 v56, v35, v58, v57
	v_med3_f32 v57, v35, v59, v58
	v_med3_f32 v58, v35, v60, v59
	v_med3_f32 v59, v35, v61, v60
	v_med3_f32 v60, v35, v62, v61
	v_med3_f32 v61, v35, v63, v62
	v_med3_f32 v62, v35, v64, v63
	v_med3_f32 v63, v35, v34, v64
	v_max_f32_e32 v35, v35, v35
	v_max_f32_e32 v34, v34, v35
	v_and_or_b32 v35, v37, s44, 19
	v_med3_f32 v36, v35, v50, v36
	v_med3_f32 v37, v35, v51, v50
	v_med3_f32 v50, v35, v52, v51
	v_med3_f32 v51, v35, v53, v52
	v_med3_f32 v52, v35, v54, v53
	v_med3_f32 v53, v35, v55, v54
	v_med3_f32 v54, v35, v56, v55
	v_med3_f32 v55, v35, v57, v56
	v_med3_f32 v56, v35, v58, v57
	v_med3_f32 v57, v35, v59, v58
	v_med3_f32 v58, v35, v60, v59
	v_med3_f32 v59, v35, v61, v60
	v_med3_f32 v60, v35, v62, v61
	v_med3_f32 v61, v35, v63, v62
	v_med3_f32 v62, v35, v34, v63
	v_max_f32_e32 v35, v35, v35
	v_max_f32_e32 v34, v34, v35
	v_and_or_b32 v35, v38, s44, 20
	v_med3_f32 v36, v35, v37, v36
	v_med3_f32 v37, v35, v50, v37
	v_med3_f32 v38, v35, v51, v50
	v_med3_f32 v50, v35, v52, v51
	v_med3_f32 v51, v35, v53, v52
	v_med3_f32 v52, v35, v54, v53
	v_med3_f32 v53, v35, v55, v54
	v_med3_f32 v54, v35, v56, v55
	v_med3_f32 v55, v35, v57, v56
	v_med3_f32 v56, v35, v58, v57
	v_med3_f32 v57, v35, v59, v58
	v_med3_f32 v58, v35, v60, v59
	v_med3_f32 v59, v35, v61, v60
	v_med3_f32 v60, v35, v62, v61
	v_med3_f32 v61, v35, v34, v62
	v_max_f32_e32 v35, v35, v35
	v_max_f32_e32 v34, v34, v35
	v_and_or_b32 v35, v39, s44, 21
	v_med3_f32 v36, v35, v37, v36
	v_med3_f32 v37, v35, v38, v37
	v_med3_f32 v38, v35, v50, v38
	v_med3_f32 v39, v35, v51, v50
	v_med3_f32 v50, v35, v52, v51
	v_med3_f32 v51, v35, v53, v52
	v_med3_f32 v52, v35, v54, v53
	v_med3_f32 v53, v35, v55, v54
	v_med3_f32 v54, v35, v56, v55
	v_med3_f32 v55, v35, v57, v56
	v_med3_f32 v56, v35, v58, v57
	v_med3_f32 v57, v35, v59, v58
	v_med3_f32 v58, v35, v60, v59
	v_med3_f32 v59, v35, v61, v60
	v_med3_f32 v60, v35, v34, v61
	v_max_f32_e32 v35, v35, v35
	v_max_f32_e32 v34, v34, v35
	v_and_or_b32 v35, v40, s44, 22
	v_med3_f32 v36, v35, v37, v36
	v_med3_f32 v37, v35, v38, v37
	v_med3_f32 v38, v35, v39, v38
	v_med3_f32 v39, v35, v50, v39
	v_med3_f32 v40, v35, v51, v50
	v_med3_f32 v50, v35, v52, v51
	v_med3_f32 v51, v35, v53, v52
	v_med3_f32 v52, v35, v54, v53
	v_med3_f32 v53, v35, v55, v54
	v_med3_f32 v54, v35, v56, v55
	v_med3_f32 v55, v35, v57, v56
	v_med3_f32 v56, v35, v58, v57
	v_med3_f32 v57, v35, v59, v58
	v_med3_f32 v58, v35, v60, v59
	v_med3_f32 v59, v35, v34, v60
	v_max_f32_e32 v35, v35, v35
	v_max_f32_e32 v34, v34, v35
	v_and_or_b32 v35, v41, s44, 23
	v_med3_f32 v36, v35, v37, v36
	v_med3_f32 v37, v35, v38, v37
	v_med3_f32 v38, v35, v39, v38
	v_med3_f32 v39, v35, v40, v39
	v_med3_f32 v40, v35, v50, v40
	v_med3_f32 v41, v35, v51, v50
	v_med3_f32 v50, v35, v52, v51
	v_med3_f32 v51, v35, v53, v52
	v_med3_f32 v52, v35, v54, v53
	v_med3_f32 v53, v35, v55, v54
	v_med3_f32 v54, v35, v56, v55
	v_med3_f32 v55, v35, v57, v56
	v_med3_f32 v56, v35, v58, v57
	v_med3_f32 v57, v35, v59, v58
	v_med3_f32 v58, v35, v34, v59
	v_max_f32_e32 v35, v35, v35
	v_max_f32_e32 v34, v34, v35
	v_and_or_b32 v35, v42, s44, 24
	v_med3_f32 v36, v35, v37, v36
	v_med3_f32 v37, v35, v38, v37
	v_med3_f32 v38, v35, v39, v38
	v_med3_f32 v39, v35, v40, v39
	v_med3_f32 v40, v35, v41, v40
	v_med3_f32 v41, v35, v50, v41
	v_med3_f32 v42, v35, v51, v50
	v_med3_f32 v50, v35, v52, v51
	v_med3_f32 v51, v35, v53, v52
	v_med3_f32 v52, v35, v54, v53
	v_med3_f32 v53, v35, v55, v54
	v_med3_f32 v54, v35, v56, v55
	v_med3_f32 v55, v35, v57, v56
	v_med3_f32 v56, v35, v58, v57
	v_med3_f32 v57, v35, v34, v58
	v_max_f32_e32 v35, v35, v35
	v_max_f32_e32 v34, v34, v35
	v_and_or_b32 v35, v43, s44, 25
	v_med3_f32 v36, v35, v37, v36
	v_med3_f32 v37, v35, v38, v37
	v_med3_f32 v38, v35, v39, v38
	v_med3_f32 v39, v35, v40, v39
	v_med3_f32 v40, v35, v41, v40
	v_med3_f32 v41, v35, v42, v41
	v_med3_f32 v42, v35, v50, v42
	v_med3_f32 v43, v35, v51, v50
	v_med3_f32 v50, v35, v52, v51
	v_med3_f32 v51, v35, v53, v52
	v_med3_f32 v52, v35, v54, v53
; DI int crow(int reg, int h) { return (reg & 3) + 8 * (reg >> 2) + 4 * h; }
; DI void topk_insert(float (&L)[16], float x) {
; #pragma unroll
;     for (int i = 15; i >= 1; --i) L[i] = __builtin_amdgcn_fmed3f(x, L[i - 1], L[i]);
;     L[0] = fmaxf(L[0], x);
; }
; DI void p8_phase(Frame& F) {
;     ...
;             for (int kt = 0; kt < 4; ++kt) {
;                 if (kt == 2) { trow_finish2(F, q0 * NGWT + gcT, (q0 + 1) * NGWT + gcT, ra, rb); trow_load(F, (q0 + 2) * NGWT + gcT, ra); trow_load(F, (q0 + 3) * NGWT + gcT, rb); }
; #pragma unroll
;                 for (int reg = 0; reg < 16; ++reg) { const unsigned key = (unsigned)(kt * 32 + crow(reg, h)); const float sv = acc[kt][reg];
;                     topk_insert(L, __uint_as_float((__float_as_uint(sv) & ~127u) | key)); }
	v_med3_f32 v53, v35, v55, v54
	v_med3_f32 v54, v35, v56, v55
	v_med3_f32 v55, v35, v57, v56
	v_med3_f32 v56, v35, v34, v57
	v_max_f32_e32 v35, v35, v35
	v_max_f32_e32 v34, v34, v35
	v_and_or_b32 v35, v44, s44, 26
	v_med3_f32 v36, v35, v37, v36
	v_med3_f32 v37, v35, v38, v37
	v_med3_f32 v38, v35, v39, v38
	v_med3_f32 v39, v35, v40, v39
	v_med3_f32 v40, v35, v41, v40
	v_med3_f32 v41, v35, v42, v41
	v_med3_f32 v42, v35, v43, v42
	v_med3_f32 v43, v35, v50, v43
	v_med3_f32 v44, v35, v51, v50
	v_med3_f32 v50, v35, v52, v51
	v_med3_f32 v51, v35, v53, v52
	v_med3_f32 v52, v35, v54, v53
	v_med3_f32 v53, v35, v55, v54
	v_med3_f32 v54, v35, v56, v55
	v_med3_f32 v55, v35, v34, v56
	v_max_f32_e32 v35, v35, v35
	v_max_f32_e32 v34, v34, v35
	v_and_or_b32 v35, v45, s44, 27
	v_med3_f32 v36, v35, v37, v36
	v_med3_f32 v37, v35, v38, v37
	v_med3_f32 v38, v35, v39, v38
	v_med3_f32 v39, v35, v40, v39
	v_med3_f32 v40, v35, v41, v40
	v_med3_f32 v41, v35, v42, v41
	v_med3_f32 v42, v35, v43, v42
	v_med3_f32 v43, v35, v44, v43
	v_med3_f32 v44, v35, v50, v44
	v_med3_f32 v45, v35, v51, v50
	v_med3_f32 v50, v35, v52, v51
	v_med3_f32 v51, v35, v53, v52
	v_med3_f32 v52, v35, v54, v53
	v_med3_f32 v53, v35, v55, v54
	v_med3_f32 v54, v35, v34, v55
	v_max_f32_e32 v35, v35, v35
	v_max_f32_e32 v34, v34, v35
	v_and_or_b32 v35, v46, s44, 28
	v_med3_f32 v36, v35, v37, v36
	v_med3_f32 v37, v35, v38, v37
	v_med3_f32 v38, v35, v39, v38
	v_med3_f32 v39, v35, v40, v39
	v_med3_f32 v40, v35, v41, v40
	v_med3_f32 v41, v35, v42, v41
	v_med3_f32 v42, v35, v43, v42
	v_med3_f32 v43, v35, v44, v43
	v_med3_f32 v44, v35, v45, v44
	v_med3_f32 v45, v35, v50, v45
	v_med3_f32 v46, v35, v51, v50
	v_med3_f32 v50, v35, v52, v51
	v_med3_f32 v51, v35, v53, v52
	v_med3_f32 v52, v35, v54, v53
	v_med3_f32 v53, v35, v34, v54
	v_max_f32_e32 v35, v35, v35
	v_max_f32_e32 v34, v34, v35
	v_and_or_b32 v35, v47, s44, 29
	v_med3_f32 v36, v35, v37, v36
	v_med3_f32 v37, v35, v38, v37
	v_med3_f32 v38, v35, v39, v38
	v_med3_f32 v39, v35, v40, v39
	v_med3_f32 v40, v35, v41, v40
	v_med3_f32 v41, v35, v42, v41
	v_med3_f32 v42, v35, v43, v42
	v_med3_f32 v43, v35, v44, v43
	v_med3_f32 v44, v35, v45, v44
	v_med3_f32 v45, v35, v46, v45
	v_med3_f32 v46, v35, v50, v46
	v_med3_f32 v47, v35, v51, v50
	v_med3_f32 v50, v35, v52, v51
	v_med3_f32 v51, v35, v53, v52
	v_med3_f32 v52, v35, v34, v53
	v_max_f32_e32 v35, v35, v35
	v_max_f32_e32 v34, v34, v35
	v_and_or_b32 v35, v48, s44, 30
	v_med3_f32 v36, v35, v37, v36
	v_med3_f32 v37, v35, v38, v37
	v_med3_f32 v38, v35, v39, v38
	v_med3_f32 v39, v35, v40, v39
	v_med3_f32 v40, v35, v41, v40
	v_med3_f32 v41, v35, v42, v41
	v_med3_f32 v42, v35, v43, v42
	v_med3_f32 v43, v35, v44, v43
	v_med3_f32 v44, v35, v45, v44
	v_med3_f32 v45, v35, v46, v45
	v_med3_f32 v46, v35, v47, v46
	v_med3_f32 v47, v35, v50, v47
	v_med3_f32 v48, v35, v51, v50
	v_med3_f32 v50, v35, v52, v51
	v_med3_f32 v51, v35, v34, v52
	v_max_f32_e32 v35, v35, v35
	v_max_f32_e32 v34, v34, v35
	v_and_or_b32 v35, v49, s44, 31
	v_med3_f32 v36, v35, v37, v36
	v_med3_f32 v37, v35, v38, v37
	v_med3_f32 v38, v35, v39, v38
	v_med3_f32 v39, v35, v40, v39
	v_med3_f32 v40, v35, v41, v40
	v_med3_f32 v41, v35, v42, v41
	v_med3_f32 v42, v35, v43, v42
	v_med3_f32 v43, v35, v44, v43
	v_med3_f32 v44, v35, v45, v44
	v_med3_f32 v45, v35, v46, v45
	v_med3_f32 v46, v35, v47, v46
	v_med3_f32 v47, v35, v48, v47
	v_med3_f32 v48, v35, v50, v48
	v_med3_f32 v49, v35, v51, v50
	v_med3_f32 v50, v35, v34, v51
	v_max_f32_e32 v35, v35, v35
	v_max_f32_e32 v34, v34, v35
	v_and_or_b32 v18, v18, s44, 32
	v_med3_f32 v35, v18, v37, v36
	v_med3_f32 v36, v18, v38, v37
	v_med3_f32 v37, v18, v39, v38
	v_med3_f32 v38, v18, v40, v39
	v_med3_f32 v39, v18, v41, v40
	v_med3_f32 v40, v18, v42, v41
	v_med3_f32 v41, v18, v43, v42
	v_med3_f32 v42, v18, v44, v43
	v_med3_f32 v43, v18, v45, v44
	v_med3_f32 v44, v18, v46, v45
	v_med3_f32 v45, v18, v47, v46
	v_med3_f32 v46, v18, v48, v47
	v_med3_f32 v47, v18, v49, v48
	v_med3_f32 v48, v18, v50, v49
	v_med3_f32 v49, v18, v34, v50
	v_max_f32_e32 v18, v18, v18
	v_max_f32_e32 v18, v34, v18
	v_and_or_b32 v19, v19, s44, 33
	v_med3_f32 v34, v19, v36, v35
	v_med3_f32 v35, v19, v37, v36
	v_med3_f32 v36, v19, v38, v37
	v_med3_f32 v37, v19, v39, v38
	v_med3_f32 v38, v19, v40, v39
	v_med3_f32 v39, v19, v41, v40
	v_med3_f32 v40, v19, v42, v41
	v_med3_f32 v41, v19, v43, v42
	v_med3_f32 v42, v19, v44, v43
	v_med3_f32 v43, v19, v45, v44
	v_med3_f32 v44, v19, v46, v45
	v_med3_f32 v45, v19, v47, v46
	v_med3_f32 v46, v19, v48, v47
	v_med3_f32 v47, v19, v49, v48
	v_med3_f32 v48, v19, v18, v49
	v_max_f32_e32 v19, v19, v19
	v_max_f32_e32 v18, v18, v19
	v_and_or_b32 v19, v20, s44, 34
	v_med3_f32 v20, v19, v35, v34
	v_med3_f32 v34, v19, v36, v35
	v_med3_f32 v35, v19, v37, v36
	v_med3_f32 v36, v19, v38, v37
	v_med3_f32 v37, v19, v39, v38
	v_med3_f32 v38, v19, v40, v39
	v_med3_f32 v39, v19, v41, v40
	v_med3_f32 v40, v19, v42, v41
	v_med3_f32 v41, v19, v43, v42
	v_med3_f32 v42, v19, v44, v43
	v_med3_f32 v43, v19, v45, v44
	v_med3_f32 v44, v19, v46, v45
	v_med3_f32 v45, v19, v47, v46
	v_med3_f32 v46, v19, v48, v47
	v_med3_f32 v47, v19, v18, v48
	v_max_f32_e32 v19, v19, v19
	v_max_f32_e32 v18, v18, v19
	v_and_or_b32 v19, v21, s44, 35
	v_med3_f32 v20, v19, v34, v20
	v_med3_f32 v21, v19, v35, v34
	v_med3_f32 v34, v19, v36, v35
	v_med3_f32 v35, v19, v37, v36
	v_med3_f32 v36, v19, v38, v37
	v_med3_f32 v37, v19, v39, v38
	v_med3_f32 v38, v19, v40, v39
	v_med3_f32 v39, v19, v41, v40
	v_med3_f32 v40, v19, v42, v41
	v_med3_f32 v41, v19, v43, v42
	v_med3_f32 v42, v19, v44, v43
	v_med3_f32 v43, v19, v45, v44
	v_med3_f32 v44, v19, v46, v45
	v_med3_f32 v45, v19, v47, v46
; DI int crow(int reg, int h) { return (reg & 3) + 8 * (reg >> 2) + 4 * h; }
; DI void topk_insert(float (&L)[16], float x) {
; #pragma unroll
;     for (int i = 15; i >= 1; --i) L[i] = __builtin_amdgcn_fmed3f(x, L[i - 1], L[i]);
;     L[0] = fmaxf(L[0], x);
; }
; DI void p8_phase(Frame& F) {
;     ...
;             for (int kt = 0; kt < 4; ++kt) {
;                 if (kt == 2) { trow_finish2(F, q0 * NGWT + gcT, (q0 + 1) * NGWT + gcT, ra, rb); trow_load(F, (q0 + 2) * NGWT + gcT, ra); trow_load(F, (q0 + 3) * NGWT + gcT, rb); }
; #pragma unroll
;                 for (int reg = 0; reg < 16; ++reg) { const unsigned key = (unsigned)(kt * 32 + crow(reg, h)); const float sv = acc[kt][reg];
;                     topk_insert(L, __uint_as_float((__float_as_uint(sv) & ~127u) | key)); }
;             }
	v_med3_f32 v46, v19, v18, v47
	v_max_f32_e32 v19, v19, v19
	v_max_f32_e32 v18, v18, v19
	v_and_or_b32 v19, v22, s44, 36
	v_med3_f32 v20, v19, v21, v20
	v_med3_f32 v21, v19, v34, v21
	v_med3_f32 v22, v19, v35, v34
	v_med3_f32 v34, v19, v36, v35
	v_med3_f32 v35, v19, v37, v36
	v_med3_f32 v36, v19, v38, v37
	v_med3_f32 v37, v19, v39, v38
	v_med3_f32 v38, v19, v40, v39
	v_med3_f32 v39, v19, v41, v40
	v_med3_f32 v40, v19, v42, v41
	v_med3_f32 v41, v19, v43, v42
	v_med3_f32 v42, v19, v44, v43
	v_med3_f32 v43, v19, v45, v44
	v_med3_f32 v44, v19, v46, v45
	v_med3_f32 v45, v19, v18, v46
	v_max_f32_e32 v19, v19, v19
	v_max_f32_e32 v18, v18, v19
	v_and_or_b32 v19, v23, s44, 37
	v_med3_f32 v20, v19, v21, v20
	v_med3_f32 v21, v19, v22, v21
	v_med3_f32 v22, v19, v34, v22
	v_med3_f32 v23, v19, v35, v34
	v_med3_f32 v34, v19, v36, v35
	v_med3_f32 v35, v19, v37, v36
	v_med3_f32 v36, v19, v38, v37
	v_med3_f32 v37, v19, v39, v38
	v_med3_f32 v38, v19, v40, v39
	v_med3_f32 v39, v19, v41, v40
	v_med3_f32 v40, v19, v42, v41
	v_med3_f32 v41, v19, v43, v42
	v_med3_f32 v42, v19, v44, v43
	v_med3_f32 v43, v19, v45, v44
	v_med3_f32 v44, v19, v18, v45
	v_max_f32_e32 v19, v19, v19
	v_max_f32_e32 v18, v18, v19
	v_and_or_b32 v19, v24, s44, 38
	v_med3_f32 v20, v19, v21, v20
	v_med3_f32 v21, v19, v22, v21
	v_med3_f32 v22, v19, v23, v22
	v_med3_f32 v23, v19, v34, v23
	v_med3_f32 v24, v19, v35, v34
	v_med3_f32 v34, v19, v36, v35
	v_med3_f32 v35, v19, v37, v36
	v_med3_f32 v36, v19, v38, v37
	v_med3_f32 v37, v19, v39, v38
	v_med3_f32 v38, v19, v40, v39
	v_med3_f32 v39, v19, v41, v40
	v_med3_f32 v40, v19, v42, v41
	v_med3_f32 v41, v19, v43, v42
	v_med3_f32 v42, v19, v44, v43
	v_med3_f32 v43, v19, v18, v44
	v_max_f32_e32 v19, v19, v19
	v_max_f32_e32 v18, v18, v19
	v_and_or_b32 v19, v25, s44, 39
	v_med3_f32 v20, v19, v21, v20
	v_med3_f32 v21, v19, v22, v21
	v_med3_f32 v22, v19, v23, v22
	v_med3_f32 v23, v19, v24, v23
	v_med3_f32 v24, v19, v34, v24
	v_med3_f32 v25, v19, v35, v34
	v_med3_f32 v34, v19, v36, v35
	v_med3_f32 v35, v19, v37, v36
	v_med3_f32 v36, v19, v38, v37
	v_med3_f32 v37, v19, v39, v38
	v_med3_f32 v38, v19, v40, v39
	v_med3_f32 v39, v19, v41, v40
	v_med3_f32 v40, v19, v42, v41
	v_med3_f32 v41, v19, v43, v42
	v_med3_f32 v42, v19, v18, v43
	v_max_f32_e32 v19, v19, v19
	v_max_f32_e32 v18, v18, v19
	v_and_or_b32 v19, v26, s44, 40
	v_med3_f32 v20, v19, v21, v20
	v_med3_f32 v21, v19, v22, v21
	v_med3_f32 v22, v19, v23, v22
	v_med3_f32 v23, v19, v24, v23
	v_med3_f32 v24, v19, v25, v24
	v_med3_f32 v25, v19, v34, v25
	v_med3_f32 v26, v19, v35, v34
	v_med3_f32 v34, v19, v36, v35
	v_med3_f32 v35, v19, v37, v36
	v_med3_f32 v36, v19, v38, v37
	v_med3_f32 v37, v19, v39, v38
	v_med3_f32 v38, v19, v40, v39
	v_med3_f32 v39, v19, v41, v40
	v_med3_f32 v40, v19, v42, v41
	v_med3_f32 v41, v19, v18, v42
	v_max_f32_e32 v19, v19, v19
	v_max_f32_e32 v18, v18, v19
	v_and_or_b32 v19, v27, s44, 41
	v_med3_f32 v20, v19, v21, v20
	v_med3_f32 v21, v19, v22, v21
	v_med3_f32 v22, v19, v23, v22
	v_med3_f32 v23, v19, v24, v23
	v_med3_f32 v24, v19, v25, v24
	v_med3_f32 v25, v19, v26, v25
	v_med3_f32 v26, v19, v34, v26
	v_med3_f32 v27, v19, v35, v34
	v_med3_f32 v34, v19, v36, v35
	v_med3_f32 v35, v19, v37, v36
	v_med3_f32 v36, v19, v38, v37
	v_med3_f32 v37, v19, v39, v38
	v_med3_f32 v38, v19, v40, v39
	v_med3_f32 v39, v19, v41, v40
	v_med3_f32 v40, v19, v18, v41
	v_max_f32_e32 v19, v19, v19
	v_max_f32_e32 v18, v18, v19
	v_and_or_b32 v19, v28, s44, 42
	v_med3_f32 v20, v19, v21, v20
	v_med3_f32 v21, v19, v22, v21
	v_med3_f32 v22, v19, v23, v22
	v_med3_f32 v23, v19, v24, v23
	v_med3_f32 v24, v19, v25, v24
	v_med3_f32 v25, v19, v26, v25
	v_med3_f32 v26, v19, v27, v26
	v_med3_f32 v27, v19, v34, v27
	v_med3_f32 v28, v19, v35, v34
	v_med3_f32 v34, v19, v36, v35
	v_med3_f32 v35, v19, v37, v36
	v_med3_f32 v36, v19, v38, v37
	v_med3_f32 v37, v19, v39, v38
	v_med3_f32 v38, v19, v40, v39
	v_med3_f32 v39, v19, v18, v40
	v_max_f32_e32 v19, v19, v19
	v_max_f32_e32 v18, v18, v19
	v_and_or_b32 v19, v29, s44, 43
	v_med3_f32 v20, v19, v21, v20
	v_med3_f32 v21, v19, v22, v21
	v_med3_f32 v22, v19, v23, v22
	v_med3_f32 v23, v19, v24, v23
	v_med3_f32 v24, v19, v25, v24
	v_med3_f32 v25, v19, v26, v25
	v_med3_f32 v26, v19, v27, v26
	v_med3_f32 v27, v19, v28, v27
	v_med3_f32 v28, v19, v34, v28
	v_med3_f32 v29, v19, v35, v34
	v_med3_f32 v34, v19, v36, v35
	v_med3_f32 v35, v19, v37, v36
	v_med3_f32 v36, v19, v38, v37
	v_med3_f32 v37, v19, v39, v38
	v_med3_f32 v38, v19, v18, v39
	v_max_f32_e32 v19, v19, v19
	v_max_f32_e32 v18, v18, v19
	v_and_or_b32 v19, v30, s44, 44
	v_med3_f32 v20, v19, v21, v20
	v_med3_f32 v21, v19, v22, v21
	v_med3_f32 v22, v19, v23, v22
	v_med3_f32 v23, v19, v24, v23
	v_med3_f32 v24, v19, v25, v24
	v_med3_f32 v25, v19, v26, v25
	v_med3_f32 v26, v19, v27, v26
	v_med3_f32 v27, v19, v28, v27
	v_med3_f32 v28, v19, v29, v28
	v_med3_f32 v29, v19, v34, v29
	v_med3_f32 v30, v19, v35, v34
	v_med3_f32 v34, v19, v36, v35
	v_med3_f32 v35, v19, v37, v36
	v_med3_f32 v36, v19, v38, v37
	v_med3_f32 v37, v19, v18, v38
	v_max_f32_e32 v19, v19, v19
	v_max_f32_e32 v18, v18, v19
	v_and_or_b32 v19, v31, s44, 45
	v_med3_f32 v20, v19, v21, v20
	v_med3_f32 v21, v19, v22, v21
	v_med3_f32 v22, v19, v23, v22
	v_med3_f32 v23, v19, v24, v23
	v_med3_f32 v24, v19, v25, v24
	v_med3_f32 v25, v19, v26, v25
	v_med3_f32 v26, v19, v27, v26
	v_med3_f32 v27, v19, v28, v27
	v_med3_f32 v28, v19, v29, v28
	v_med3_f32 v29, v19, v30, v29
	v_med3_f32 v30, v19, v34, v30
	v_med3_f32 v31, v19, v35, v34
	v_med3_f32 v34, v19, v36, v35
	v_med3_f32 v35, v19, v37, v36
	v_med3_f32 v36, v19, v18, v37
	v_max_f32_e32 v19, v19, v19
	v_max_f32_e32 v18, v18, v19
	v_and_or_b32 v19, v32, s44, 46
	v_med3_f32 v20, v19, v21, v20
	v_med3_f32 v21, v19, v22, v21
	v_med3_f32 v22, v19, v23, v22
	v_med3_f32 v23, v19, v24, v23
	v_med3_f32 v24, v19, v25, v24
	v_med3_f32 v25, v19, v26, v25
	v_med3_f32 v26, v19, v27, v26
	v_med3_f32 v27, v19, v28, v27
	v_med3_f32 v28, v19, v29, v28
	v_med3_f32 v29, v19, v30, v29
	v_med3_f32 v30, v19, v31, v30
	v_med3_f32 v31, v19, v34, v31
	v_med3_f32 v32, v19, v35, v34
	v_med3_f32 v34, v19, v36, v35
	v_med3_f32 v35, v19, v18, v36
	v_max_f32_e32 v19, v19, v19
	v_max_f32_e32 v18, v18, v19
	v_and_or_b32 v19, v33, s44, 47
	v_med3_f32 v20, v19, v21, v20
	v_med3_f32 v21, v19, v22, v21
	v_med3_f32 v22, v19, v23, v22
	v_med3_f32 v23, v19, v24, v23
	v_med3_f32 v24, v19, v25, v24
	v_med3_f32 v25, v19, v26, v25
	v_med3_f32 v26, v19, v27, v26
	v_med3_f32 v27, v19, v28, v27
	v_med3_f32 v28, v19, v29, v28
	v_med3_f32 v29, v19, v30, v29
	v_med3_f32 v30, v19, v31, v30
	v_med3_f32 v31, v19, v32, v31
	v_med3_f32 v32, v19, v34, v32
	v_med3_f32 v33, v19, v35, v34
	v_med3_f32 v34, v19, v18, v35
	v_max_f32_e32 v19, v19, v19
	v_max_f32_e32 v18, v18, v19
; #define GAS __attribute__((address_space(1)))
; DI float lane_bcast(float v, int l) { return __uint_as_float((unsigned)__builtin_amdgcn_readlane((int)__float_as_uint(v), l)); }
; DI void trow_store(Frame& F, int row, const f32x4 (&v)[8], float am) {
;     if (row >= 2 * NEXP) return;
;     const int tb = row >= NEXP, e = row - tb * NEXP; am = fmaxf(am, 1e-30f);
;     const float sc = am * (1.0f / 127.0f), inv = 127.0f / am;
;     GAS unsigned* dst = (GAS unsigned*)((tb ? F.EU : F.ED) + (size_t)e * D) + F.lane;
;     const int off = 0;
; #pragma unroll
;     for (int j = 0; j < 8; ++j) {
;         const int q0 = (int)__builtin_rintf(v[j].x * inv) + off, q1 = (int)__builtin_rintf(v[j].y * inv) + off, q2 = (int)__builtin_rintf(v[j].z * inv) + off, q3 = (int)__builtin_rintf(v[j].w * inv) + off;
; #pragma unroll
;     for (int j = 0; j < 8; ++j) am = fmaxf(am, fmaxf(fmaxf(fabsf(v[j].x), fabsf(v[j].y)), fmaxf(fabsf(v[j].z), fabsf(v[j].w))));
;     return am; }
; DI void trow_finish2(Frame& F, int rowA, int rowB, const f32x4 (&a)[8], const f32x4 (&b)[8]) {
;     const float m = red2_max(trow_absmax(a), trow_absmax(b));
;     trow_store(F, rowA, a, lane_bcast(m, 0)); trow_store(F, rowB, b, lane_bcast(m, 32));
.LBB0_1212:
	s_waitcnt vmcnt(7)
	v_max_f32_e64 v135, |v251|, |v251|
	v_max_f32_e64 v229, |v250|, |v250|
	v_max_f32_e32 v135, v229, v135
	s_waitcnt vmcnt(6)
	v_max_f32_e64 v229, |v247|, |v247|
	v_max_f32_e64 v230, |v246|, |v246|
	v_max_f32_e32 v229, v230, v229
	v_max3_f32 v135, |v248|, |v249|, v135
	v_max3_f32 v229, |v244|, |v245|, v229
	v_max3_f32 v135, v135, 0, v229
	s_waitcnt vmcnt(5)
	v_max_f32_e64 v229, |v209|, |v209|
	v_max_f32_e64 v230, |v208|, |v208|
	v_max_f32_e32 v229, v230, v229
	s_waitcnt vmcnt(4)
	v_max_f32_e64 v230, |v195|, |v195|
	v_max_f32_e64 v231, |v194|, |v194|
	v_max_f32_e32 v230, v231, v230
	v_max3_f32 v229, |v206|, |v207|, v229
	v_max3_f32 v230, |v192|, |v193|, v230
	v_max3_f32 v135, v135, v229, v230
	s_waitcnt vmcnt(3)
	v_max_f32_e64 v229, |v187|, |v187|
	v_max_f32_e64 v230, |v186|, |v186|
	v_max_f32_e32 v229, v230, v229
	s_waitcnt vmcnt(2)
	v_max_f32_e64 v230, |v179|, |v179|
	v_max_f32_e64 v231, |v178|, |v178|
	v_max_f32_e32 v230, v231, v230
	v_max3_f32 v229, |v184|, |v185|, v229
	v_max3_f32 v230, |v176|, |v177|, v230
	v_max3_f32 v135, v135, v229, v230
	s_waitcnt vmcnt(1)
	v_max_f32_e64 v229, |v167|, |v167|
	v_max_f32_e64 v230, |v166|, |v166|
	v_max_f32_e32 v229, v230, v229
	s_waitcnt vmcnt(0)
	v_max_f32_e64 v230, |v175|, |v175|
	v_max_f32_e64 v231, |v174|, |v174|
	v_max_f32_e32 v230, v231, v230
	v_max3_f32 v229, |v164|, |v165|, v229
	v_max3_f32 v230, |v172|, |v173|, v230
	v_max3_f32 v135, v135, v229, v230
	v_max_f32_e64 v229, |v213|, |v213|
	v_max_f32_e64 v230, |v212|, |v212|
	v_max_f32_e32 v229, v230, v229
	v_max_f32_e64 v230, |v205|, |v205|
	v_max_f32_e64 v231, |v204|, |v204|
	v_max_f32_e32 v230, v231, v230
	v_max3_f32 v229, |v210|, |v211|, v229
	v_max3_f32 v230, |v202|, |v203|, v230
	v_max3_f32 v229, v229, 0, v230
	v_max_f32_e64 v230, |v191|, |v191|
	v_max_f32_e64 v231, |v190|, |v190|
	v_max_f32_e32 v230, v231, v230
	v_max_f32_e64 v231, |v183|, |v183|
	v_max_f32_e64 v232, |v182|, |v182|
	v_max_f32_e32 v231, v232, v231
	v_max3_f32 v230, |v188|, |v189|, v230
	v_max3_f32 v231, |v180|, |v181|, v231
	v_max3_f32 v229, v229, v230, v231
	v_max_f32_e64 v230, |v171|, |v171|
	v_max_f32_e64 v231, |v170|, |v170|
	v_max_f32_e32 v230, v231, v230
	v_max_f32_e64 v231, |v163|, |v163|
	v_max_f32_e64 v232, |v162|, |v162|
	v_max_f32_e32 v231, v232, v231
	v_max3_f32 v230, |v168|, |v169|, v230
	v_max3_f32 v231, |v160|, |v161|, v231
	v_max3_f32 v229, v229, v230, v231
	v_max_f32_e64 v230, |v155|, |v155|
	v_max_f32_e64 v231, |v154|, |v154|
	v_max_f32_e32 v230, v231, v230
	v_max_f32_e64 v231, |v159|, |v159|
	v_max_f32_e64 v232, |v158|, |v158|
	v_max_f32_e32 v231, v232, v231
	v_max3_f32 v230, |v152|, |v153|, v230
	v_max3_f32 v231, |v156|, |v157|, v231
	v_max3_f32 v229, v229, v230, v231
	s_nop 1
	v_permlane32_swap_b32_e32 v135, v229
	v_max_f32_e32 v229, v229, v229
	v_max_f32_e32 v135, v135, v135
	v_max_f32_e32 v135, v135, v229
	v_mov_b32_e32 v229, v135
	s_nop 1
	v_permlane16_swap_b32_e32 v135, v229
	v_max_f32_e32 v229, v229, v229
	v_max_f32_e32 v135, v135, v135
	v_max_f32_e32 v135, v135, v229
	s_cmpk_gt_i32 s90, 0x7fff
	s_nop 0
	v_mov_b32_dpp v229, v135 row_ror:8 row_mask:0xf bank_mask:0xf bound_ctrl:1
	v_max_f32_e32 v229, v229, v229
	v_max_f32_e32 v135, v135, v229
	s_nop 1
	v_mov_b32_dpp v229, v135 row_half_mirror row_mask:0xf bank_mask:0xf bound_ctrl:1
	v_max_f32_e32 v229, v229, v229
	v_max_f32_e32 v135, v135, v229
	s_nop 1
	v_mov_b32_dpp v229, v135 quad_perm:[1,0,3,2] row_mask:0xf bank_mask:0xf bound_ctrl:1
	v_max_f32_e32 v229, v229, v229
	v_max_f32_e32 v135, v135, v229
	s_nop 1
	v_mov_b32_dpp v229, v135 quad_perm:[2,3,0,1] row_mask:0xf bank_mask:0xf bound_ctrl:1
	v_max_f32_e32 v229, v229, v229
	v_max_f32_e32 v229, v135, v229
	v_lshlrev_b32_e32 v135, 2, v148
	v_readlane_b32 s94, v229, 0
	s_cbranch_scc1 .LBB0_1216
	s_nop 0
	v_max_f32_e64 v230, s94, s94
	v_max_f32_e32 v230, 0xda24260, v230
	v_div_scale_f32 v231, s[94:95], v230, v230, s42
	v_rcp_f32_e32 v232, v231
	s_cmpk_gt_i32 s90, 0x3fff
	s_cselect_b64 s[92:93], -1, 0
	s_and_b64 s[96:97], s[92:93], exec
	v_fma_f32 v233, -v231, v232, 1.0
	v_fmac_f32_e32 v232, v233, v232
	v_div_scale_f32 v233, vcc, s42, v230, s42
	v_mul_f32_e32 v234, v233, v232
	v_fma_f32 v235, -v231, v234, v233
	v_fmac_f32_e32 v234, v235, v232
	v_fma_f32 v231, -v231, v234, v233
	v_div_fmas_f32 v231, v231, v232, v234
	v_div_fixup_f32 v231, v231, v230, s42
	v_mul_f32_e32 v165, v165, v231
	v_mul_f32_e32 v164, v164, v231
	v_rndne_f32_e32 v165, v165
	v_mul_f32_e32 v166, v166, v231
	v_mul_f32_e32 v167, v167, v231
	v_rndne_f32_e32 v164, v164
	v_cvt_i32_f32_e32 v165, v165
	v_rndne_f32_e32 v166, v166
	v_rndne_f32_e32 v167, v167
	s_cselect_b32 s96, 0xffffc000, 0
	v_cvt_i32_f32_e32 v164, v164
	v_cvt_i32_f32_sdwa v166, v166 dst_sel:WORD_1 dst_unused:UNUSED_PAD src0_sel:DWORD
	v_cvt_i32_f32_e32 v167, v167
	s_cselect_b32 s86, s19, s39
	s_cselect_b32 s87, s18, s37
	s_add_i32 s94, s96, s90
	s_ashr_i32 s95, s94, 31
	s_lshl_b64 s[96:97], s[94:95], 11
	v_lshlrev_b32_e32 v165, 8, v165
	s_add_u32 s96, s87, s96
	v_and_b32_e32 v165, 0xff00, v165
	v_and_b32_e32 v166, 0xff0000, v166
	v_perm_b32 v164, v167, v164, s43
	s_addc_u32 s97, s86, s97
	v_mul_f32_e32 v249, v249, v231
	v_mul_f32_e32 v245, v245, v231
	v_mul_f32_e32 v207, v207, v231
	v_mul_f32_e32 v193, v193, v231
	v_mul_f32_e32 v185, v185, v231
	v_mul_f32_e32 v177, v177, v231
	v_or3_b32 v164, v164, v165, v166
	v_mul_f32_e32 v165, v173, v231
	v_mul_f32_e32 v248, v248, v231
	v_rndne_f32_e32 v249, v249
	v_mul_f32_e32 v250, v250, v231
	v_mul_f32_e32 v251, v251, v231
	v_mul_f32_e32 v244, v244, v231
	v_rndne_f32_e32 v245, v245
	v_mul_f32_e32 v246, v246, v231
	v_mul_f32_e32 v247, v247, v231
; #define GAS __attribute__((address_space(1)))
; DI void trow_store(Frame& F, int row, const f32x4 (&v)[8], float am) {
;     if (row >= 2 * NEXP) return;
;     const int tb = row >= NEXP, e = row - tb * NEXP; am = fmaxf(am, 1e-30f);
;     const float sc = am * (1.0f / 127.0f), inv = 127.0f / am;
;     GAS unsigned* dst = (GAS unsigned*)((tb ? F.EU : F.ED) + (size_t)e * D) + F.lane;
;     const int off = 0;
; #pragma unroll
;     for (int j = 0; j < 8; ++j) {
;         const int q0 = (int)__builtin_rintf(v[j].x * inv) + off, q1 = (int)__builtin_rintf(v[j].y * inv) + off, q2 = (int)__builtin_rintf(v[j].z * inv) + off, q3 = (int)__builtin_rintf(v[j].w * inv) + off;
;         dst[64 * j] = (unsigned)(q0 & 255) | ((unsigned)(q1 & 255) << 8) | ((unsigned)(q2 & 255) << 16) | ((unsigned)(q3 & 255) << 24);
;     }
;     if (F.lane == 0) (tb ? F.SU : F.SD)[e] = sc;
; }
	v_mul_f32_e32 v206, v206, v231
	v_rndne_f32_e32 v207, v207
	v_mul_f32_e32 v208, v208, v231
	v_mul_f32_e32 v209, v209, v231
	v_mul_f32_e32 v192, v192, v231
	v_rndne_f32_e32 v193, v193
	v_mul_f32_e32 v194, v194, v231
	v_mul_f32_e32 v195, v195, v231
	v_mul_f32_e32 v184, v184, v231
	v_rndne_f32_e32 v185, v185
	v_mul_f32_e32 v186, v186, v231
	v_mul_f32_e32 v187, v187, v231
	v_mul_f32_e32 v176, v176, v231
	v_rndne_f32_e32 v177, v177
	v_mul_f32_e32 v178, v178, v231
	v_mul_f32_e32 v179, v179, v231
	global_store_dword v135, v164, s[96:97] offset:1536
	v_mul_f32_e32 v164, v172, v231
	v_rndne_f32_e32 v165, v165
	v_mul_f32_e32 v166, v174, v231
	v_mul_f32_e32 v167, v175, v231
	v_rndne_f32_e32 v248, v248
	v_cvt_i32_f32_e32 v249, v249
	v_rndne_f32_e32 v250, v250
	v_rndne_f32_e32 v251, v251
	v_rndne_f32_e32 v244, v244
	v_cvt_i32_f32_e32 v245, v245
	v_rndne_f32_e32 v246, v246
	v_rndne_f32_e32 v247, v247
	v_rndne_f32_e32 v206, v206
	v_cvt_i32_f32_e32 v207, v207
	v_rndne_f32_e32 v208, v208
	v_rndne_f32_e32 v209, v209
	v_rndne_f32_e32 v192, v192
	v_cvt_i32_f32_e32 v193, v193
	v_rndne_f32_e32 v194, v194
	v_rndne_f32_e32 v195, v195
	v_rndne_f32_e32 v184, v184
	v_cvt_i32_f32_e32 v185, v185
	v_rndne_f32_e32 v186, v186
	v_rndne_f32_e32 v187, v187
	v_rndne_f32_e32 v176, v176
	v_cvt_i32_f32_e32 v177, v177
	v_rndne_f32_e32 v178, v178
	v_rndne_f32_e32 v179, v179
	v_rndne_f32_e32 v164, v164
	v_cvt_i32_f32_e32 v165, v165
	v_rndne_f32_e32 v166, v166
	v_rndne_f32_e32 v167, v167
	v_cvt_i32_f32_e32 v248, v248
	v_cvt_i32_f32_sdwa v250, v250 dst_sel:WORD_1 dst_unused:UNUSED_PAD src0_sel:DWORD
	v_cvt_i32_f32_e32 v251, v251
	v_cvt_i32_f32_e32 v244, v244
	v_cvt_i32_f32_sdwa v246, v246 dst_sel:WORD_1 dst_unused:UNUSED_PAD src0_sel:DWORD
	v_cvt_i32_f32_e32 v247, v247
	v_cvt_i32_f32_e32 v206, v206
	v_cvt_i32_f32_sdwa v208, v208 dst_sel:WORD_1 dst_unused:UNUSED_PAD src0_sel:DWORD
	v_cvt_i32_f32_e32 v209, v209
	v_cvt_i32_f32_e32 v192, v192
	v_cvt_i32_f32_sdwa v194, v194 dst_sel:WORD_1 dst_unused:UNUSED_PAD src0_sel:DWORD
	v_cvt_i32_f32_e32 v195, v195
	v_cvt_i32_f32_e32 v184, v184
	v_cvt_i32_f32_sdwa v186, v186 dst_sel:WORD_1 dst_unused:UNUSED_PAD src0_sel:DWORD
	v_cvt_i32_f32_e32 v187, v187
	v_cvt_i32_f32_e32 v176, v176
	v_cvt_i32_f32_sdwa v178, v178 dst_sel:WORD_1 dst_unused:UNUSED_PAD src0_sel:DWORD
	v_cvt_i32_f32_e32 v179, v179
	v_cvt_i32_f32_e32 v164, v164
	v_cvt_i32_f32_sdwa v166, v166 dst_sel:WORD_1 dst_unused:UNUSED_PAD src0_sel:DWORD
	v_cvt_i32_f32_e32 v167, v167
	v_lshlrev_b32_e32 v249, 8, v249
	v_lshlrev_b32_e32 v245, 8, v245
	v_lshlrev_b32_e32 v207, 8, v207
	v_lshlrev_b32_e32 v193, 8, v193
	v_lshlrev_b32_e32 v185, 8, v185
	v_lshlrev_b32_e32 v177, 8, v177
	v_lshlrev_b32_e32 v165, 8, v165
	v_and_b32_e32 v249, 0xff00, v249
	v_and_b32_e32 v250, 0xff0000, v250
	v_perm_b32 v248, v251, v248, s43
	v_and_b32_e32 v245, 0xff00, v245
	v_and_b32_e32 v246, 0xff0000, v246
	v_perm_b32 v244, v247, v244, s43
	v_and_b32_e32 v207, 0xff00, v207
	v_and_b32_e32 v208, 0xff0000, v208
	v_perm_b32 v206, v209, v206, s43
	v_and_b32_e32 v193, 0xff00, v193
	v_and_b32_e32 v194, 0xff0000, v194
	v_perm_b32 v192, v195, v192, s43
	v_and_b32_e32 v185, 0xff00, v185
	v_and_b32_e32 v186, 0xff0000, v186
	v_perm_b32 v184, v187, v184, s43
	v_and_b32_e32 v177, 0xff00, v177
	v_and_b32_e32 v178, 0xff0000, v178
	v_perm_b32 v176, v179, v176, s43
	v_and_b32_e32 v165, 0xff00, v165
	v_and_b32_e32 v166, 0xff0000, v166
	v_perm_b32 v164, v167, v164, s43
	v_or3_b32 v248, v248, v249, v250
	v_or3_b32 v244, v244, v245, v246
	v_or3_b32 v206, v206, v207, v208
	v_or3_b32 v192, v192, v193, v194
	v_or3_b32 v184, v184, v185, v186
	v_or3_b32 v176, v176, v177, v178
	v_or3_b32 v164, v164, v165, v166
	global_store_dword v135, v248, s[96:97]
	global_store_dword v135, v244, s[96:97] offset:256
	global_store_dword v135, v206, s[96:97] offset:512
	global_store_dword v135, v192, s[96:97] offset:768
	global_store_dword v135, v184, s[96:97] offset:1024
	global_store_dword v135, v176, s[96:97] offset:1280
	global_store_dword v135, v164, s[96:97] offset:1792
	s_and_saveexec_b64 s[96:97], s[4:5]
	s_cbranch_execz .LBB0_1215
	s_and_b64 s[92:93], s[92:93], exec
	s_cselect_b32 s90, s25, s21
	s_cselect_b32 s86, s24, s20
	s_lshl_b64 s[92:93], s[94:95], 2
	s_add_u32 s92, s86, s92
	s_addc_u32 s93, s90, s93
	v_mul_f32_e32 v164, 0x3c010204, v230
	global_store_dword v133, v164, s[92:93]
.LBB0_1215:
	s_or_b64 exec, exec, s[96:97]
; #define GAS __attribute__((address_space(1)))
; DI void trow_store(Frame& F, int row, const f32x4 (&v)[8], float am) {
;     if (row >= 2 * NEXP) return;
;     const int tb = row >= NEXP, e = row - tb * NEXP; am = fmaxf(am, 1e-30f);
;     const float sc = am * (1.0f / 127.0f), inv = 127.0f / am;
;     GAS unsigned* dst = (GAS unsigned*)((tb ? F.EU : F.ED) + (size_t)e * D) + F.lane;
;     const int off = 0;
; #pragma unroll
;     for (int j = 0; j < 8; ++j) {
;         const int q0 = (int)__builtin_rintf(v[j].x * inv) + off, q1 = (int)__builtin_rintf(v[j].y * inv) + off, q2 = (int)__builtin_rintf(v[j].z * inv) + off, q3 = (int)__builtin_rintf(v[j].w * inv) + off;
;         dst[64 * j] = (unsigned)(q0 & 255) | ((unsigned)(q1 & 255) << 8) | ((unsigned)(q2 & 255) << 16) | ((unsigned)(q3 & 255) << 24);
;     }
;     if (F.lane == 0) (tb ? F.SU : F.SD)[e] = sc;
; }
.LBB0_1216:
	s_cmpk_gt_i32 s91, 0x7fff
	v_readlane_b32 s90, v229, 32
	s_cbranch_scc1 .LP7_fin_b
	s_nop 0
	v_max_f32_e64 v164, s90, s90
	v_max_f32_e32 v164, 0xda24260, v164
	v_div_scale_f32 v165, s[94:95], v164, v164, s42
	v_rcp_f32_e32 v166, v165
	s_cmpk_gt_i32 s91, 0x3fff
	s_cselect_b64 s[92:93], -1, 0
	s_and_b64 s[94:95], s[92:93], exec
	v_fma_f32 v167, -v165, v166, 1.0
	v_fmac_f32_e32 v166, v167, v166
	v_div_scale_f32 v167, vcc, s42, v164, s42
	v_mul_f32_e32 v172, v167, v166
	v_fma_f32 v173, -v165, v172, v167
	v_fmac_f32_e32 v172, v173, v166
	v_fma_f32 v165, -v165, v172, v167
	v_div_fmas_f32 v165, v165, v166, v172
	v_div_fixup_f32 v165, v165, v164, s42
	v_mul_f32_e32 v167, v211, v165
	v_mul_f32_e32 v166, v210, v165
	v_rndne_f32_e32 v167, v167
	v_mul_f32_e32 v172, v212, v165
	v_mul_f32_e32 v173, v213, v165
	v_rndne_f32_e32 v166, v166
	v_cvt_i32_f32_e32 v167, v167
	v_rndne_f32_e32 v172, v172
	v_rndne_f32_e32 v173, v173
	s_cselect_b32 s96, 0xffffc000, 0
	v_cvt_i32_f32_e32 v166, v166
	v_cvt_i32_f32_sdwa v172, v172 dst_sel:WORD_1 dst_unused:UNUSED_PAD src0_sel:DWORD
	v_cvt_i32_f32_e32 v173, v173
	s_cselect_b32 s86, s19, s39
	s_cselect_b32 s90, s18, s37
	s_add_i32 s94, s96, s91
	s_ashr_i32 s95, s94, 31
	s_lshl_b64 s[96:97], s[94:95], 11
	v_lshlrev_b32_e32 v167, 8, v167
	s_add_u32 s96, s90, s96
	v_and_b32_e32 v167, 0xff00, v167
	v_and_b32_e32 v172, 0xff0000, v172
	v_perm_b32 v166, v173, v166, s43
	s_addc_u32 s97, s86, s97
	v_or3_b32 v166, v166, v167, v172
	v_mul_f32_e32 v167, v203, v165
	global_store_dword v135, v166, s[96:97]
	v_mul_f32_e32 v166, v202, v165
	v_rndne_f32_e32 v167, v167
	v_mul_f32_e32 v172, v204, v165
	v_mul_f32_e32 v173, v205, v165
	v_rndne_f32_e32 v166, v166
	v_cvt_i32_f32_e32 v167, v167
	v_rndne_f32_e32 v172, v172
	v_rndne_f32_e32 v173, v173
	v_cvt_i32_f32_e32 v166, v166
	v_cvt_i32_f32_sdwa v172, v172 dst_sel:WORD_1 dst_unused:UNUSED_PAD src0_sel:DWORD
	v_cvt_i32_f32_e32 v173, v173
	v_lshlrev_b32_e32 v167, 8, v167
	v_and_b32_e32 v167, 0xff00, v167
	v_and_b32_e32 v172, 0xff0000, v172
	v_perm_b32 v166, v173, v166, s43
	v_or3_b32 v166, v166, v167, v172
	v_mul_f32_e32 v167, v189, v165
	global_store_dword v135, v166, s[96:97] offset:256
	v_mul_f32_e32 v166, v188, v165
	v_rndne_f32_e32 v167, v167
	v_mul_f32_e32 v172, v190, v165
	v_mul_f32_e32 v173, v191, v165
	v_rndne_f32_e32 v166, v166
	v_cvt_i32_f32_e32 v167, v167
	v_rndne_f32_e32 v172, v172
	v_rndne_f32_e32 v173, v173
	v_cvt_i32_f32_e32 v166, v166
	v_cvt_i32_f32_sdwa v172, v172 dst_sel:WORD_1 dst_unused:UNUSED_PAD src0_sel:DWORD
	v_cvt_i32_f32_e32 v173, v173
	v_lshlrev_b32_e32 v167, 8, v167
	v_and_b32_e32 v167, 0xff00, v167
	v_and_b32_e32 v172, 0xff0000, v172
	v_perm_b32 v166, v173, v166, s43
	v_or3_b32 v166, v166, v167, v172
	v_mul_f32_e32 v167, v181, v165
	v_mul_f32_e32 v153, v153, v165
	global_store_dword v135, v166, s[96:97] offset:512
	v_mul_f32_e32 v166, v180, v165
	v_rndne_f32_e32 v167, v167
	v_mul_f32_e32 v172, v182, v165
	v_mul_f32_e32 v173, v183, v165
	v_mul_f32_e32 v152, v152, v165
	v_rndne_f32_e32 v153, v153
	v_mul_f32_e32 v154, v154, v165
	v_mul_f32_e32 v155, v155, v165
	v_rndne_f32_e32 v166, v166
	v_cvt_i32_f32_e32 v167, v167
	v_rndne_f32_e32 v172, v172
	v_rndne_f32_e32 v173, v173
	v_rndne_f32_e32 v152, v152
	v_cvt_i32_f32_e32 v153, v153
	v_rndne_f32_e32 v154, v154
	v_rndne_f32_e32 v155, v155
	v_cvt_i32_f32_e32 v166, v166
	v_cvt_i32_f32_sdwa v172, v172 dst_sel:WORD_1 dst_unused:UNUSED_PAD src0_sel:DWORD
	v_cvt_i32_f32_e32 v173, v173
	v_cvt_i32_f32_e32 v152, v152
	v_cvt_i32_f32_sdwa v154, v154 dst_sel:WORD_1 dst_unused:UNUSED_PAD src0_sel:DWORD
	v_cvt_i32_f32_e32 v155, v155
	v_lshlrev_b32_e32 v167, 8, v167
	v_lshlrev_b32_e32 v153, 8, v153
	v_and_b32_e32 v167, 0xff00, v167
	v_and_b32_e32 v172, 0xff0000, v172
	v_perm_b32 v166, v173, v166, s43
	v_and_b32_e32 v153, 0xff00, v153
	v_and_b32_e32 v154, 0xff0000, v154
	v_perm_b32 v152, v155, v152, s43
	v_or3_b32 v166, v166, v167, v172
	v_mul_f32_e32 v167, v169, v165
	v_mul_f32_e32 v161, v161, v165
	v_or3_b32 v152, v152, v153, v154
	v_mul_f32_e32 v153, v157, v165
	global_store_dword v135, v166, s[96:97] offset:768
	v_mul_f32_e32 v166, v168, v165
	v_rndne_f32_e32 v167, v167
	v_mul_f32_e32 v168, v170, v165
	v_mul_f32_e32 v169, v171, v165
	v_mul_f32_e32 v160, v160, v165
	v_rndne_f32_e32 v161, v161
	v_mul_f32_e32 v162, v162, v165
	v_mul_f32_e32 v163, v163, v165
	global_store_dword v135, v152, s[96:97] offset:1536
	v_mul_f32_e32 v152, v156, v165
	v_rndne_f32_e32 v153, v153
	v_mul_f32_e32 v154, v158, v165
	v_mul_f32_e32 v155, v159, v165
	v_rndne_f32_e32 v166, v166
	v_cvt_i32_f32_e32 v167, v167
	v_rndne_f32_e32 v168, v168
	v_rndne_f32_e32 v169, v169
	v_rndne_f32_e32 v160, v160
	v_cvt_i32_f32_e32 v161, v161
	v_rndne_f32_e32 v162, v162
	v_rndne_f32_e32 v163, v163
	v_rndne_f32_e32 v152, v152
	v_cvt_i32_f32_e32 v153, v153
	v_rndne_f32_e32 v154, v154
	v_rndne_f32_e32 v155, v155
	v_cvt_i32_f32_e32 v166, v166
	v_cvt_i32_f32_sdwa v168, v168 dst_sel:WORD_1 dst_unused:UNUSED_PAD src0_sel:DWORD
	v_cvt_i32_f32_e32 v169, v169
	v_cvt_i32_f32_e32 v160, v160
	v_cvt_i32_f32_sdwa v162, v162 dst_sel:WORD_1 dst_unused:UNUSED_PAD src0_sel:DWORD
	v_cvt_i32_f32_e32 v163, v163
	v_cvt_i32_f32_e32 v152, v152
	v_cvt_i32_f32_sdwa v154, v154 dst_sel:WORD_1 dst_unused:UNUSED_PAD src0_sel:DWORD
	v_cvt_i32_f32_e32 v155, v155
	v_lshlrev_b32_e32 v167, 8, v167
	v_lshlrev_b32_e32 v161, 8, v161
	v_lshlrev_b32_e32 v153, 8, v153
	v_and_b32_e32 v167, 0xff00, v167
	v_and_b32_e32 v168, 0xff0000, v168
	v_perm_b32 v166, v169, v166, s43
	v_and_b32_e32 v161, 0xff00, v161
	v_and_b32_e32 v162, 0xff0000, v162
	v_perm_b32 v160, v163, v160, s43
	v_and_b32_e32 v153, 0xff00, v153
	v_and_b32_e32 v154, 0xff0000, v154
	v_perm_b32 v152, v155, v152, s43
	v_or3_b32 v166, v166, v167, v168
	v_or3_b32 v160, v160, v161, v162
	v_or3_b32 v152, v152, v153, v154
	global_store_dword v135, v166, s[96:97] offset:1024
	global_store_dword v135, v160, s[96:97] offset:1280
	global_store_dword v135, v152, s[96:97] offset:1792
	s_and_saveexec_b64 s[96:97], s[4:5]
	s_cbranch_execz .LBB0_1219
	s_and_b64 s[92:93], s[92:93], exec
	s_cselect_b32 s90, s25, s21
	s_cselect_b32 s86, s24, s20
	s_lshl_b64 s[92:93], s[94:95], 2
	s_add_u32 s92, s86, s92
	s_addc_u32 s93, s90, s93
	v_mul_f32_e32 v152, 0x3c010204, v164
	global_store_dword v133, v152, s[92:93]

; DI int crow(int reg, int h) { return (reg & 3) + 8 * (reg >> 2) + 4 * h; }
; #pragma unroll
;     for (int j = 0; j < 8; ++j) am = fmaxf(am, fmaxf(fmaxf(fabsf(v[j].x), fabsf(v[j].y)), fmaxf(fabsf(v[j].z), fabsf(v[j].w))));
;     return am; }
; DI void trow_finish2(Frame& F, int rowA, int rowB, const f32x4 (&a)[8], const f32x4 (&b)[8]) {
;     const float m = red2_max(trow_absmax(a), trow_absmax(b));
; DI void p8_phase(Frame& F) {
;     ...
;             for (int kt = 0; kt < 4; ++kt) {
;                 if (kt == 2) { trow_finish2(F, q0 * NGWT + gcT, (q0 + 1) * NGWT + gcT, ra, rb); trow_load(F, (q0 + 2) * NGWT + gcT, ra); trow_load(F, (q0 + 3) * NGWT + gcT, rb); }
; #pragma unroll
;                 for (int reg = 0; reg < 16; ++reg) { const unsigned key = (unsigned)(kt * 32 + crow(reg, h)); const float sv = acc[kt][reg];
;                     topk_insert(L, __uint_as_float((__float_as_uint(sv) & ~127u) | key)); }
;             }
.LP7_fin_b:
	v_max_f32_e64 v19, |v121|, |v121|
	v_max_f32_e64 v35, |v120|, |v120|
	v_max_f32_e32 v19, v35, v19
	v_max_f32_e64 v35, |v113|, |v113|
	v_max_f32_e64 v36, |v112|, |v112|
	v_max_f32_e32 v35, v36, v35
	v_max3_f32 v19, |v118|, |v119|, v19
	v_max3_f32 v35, |v110|, |v111|, v35
	v_max3_f32 v19, v19, 0, v35
	v_max_f32_e64 v35, |v105|, |v105|
	v_max_f32_e64 v36, |v104|, |v104|
	v_max_f32_e32 v35, v36, v35
	v_max_f32_e64 v36, |v97|, |v97|
	v_max_f32_e64 v37, |v96|, |v96|
	v_max_f32_e32 v36, v37, v36
	v_max3_f32 v35, |v102|, |v103|, v35
	v_max3_f32 v36, |v94|, |v95|, v36
	v_max3_f32 v19, v19, v35, v36
	v_max_f32_e64 v35, |v89|, |v89|
	v_max_f32_e64 v36, |v88|, |v88|
	v_max_f32_e32 v35, v36, v35
	v_max_f32_e64 v36, |v77|, |v77|
	v_max_f32_e64 v37, |v76|, |v76|
	v_max_f32_e32 v36, v37, v36
	v_max3_f32 v35, |v86|, |v87|, v35
	v_max3_f32 v36, |v74|, |v75|, v36
	v_max3_f32 v19, v19, v35, v36
	v_max_f32_e64 v35, |v73|, |v73|
	v_max_f32_e64 v36, |v72|, |v72|
	v_max_f32_e32 v35, v36, v35
	v_max_f32_e64 v36, |v69|, |v69|
	v_max_f32_e64 v37, |v68|, |v68|
	v_max_f32_e32 v36, v37, v36
	v_max3_f32 v35, |v70|, |v71|, v35
	v_max3_f32 v36, |v66|, |v67|, v36
	v_max3_f32 v35, v19, v35, v36
	v_max_f32_e64 v19, |v129|, |v129|
	v_max_f32_e64 v36, |v128|, |v128|
	v_max_f32_e32 v19, v36, v19
	v_max_f32_e64 v36, |v125|, |v125|
	v_max_f32_e64 v37, |v124|, |v124|
	v_max_f32_e32 v36, v37, v36
	v_max3_f32 v19, |v126|, |v127|, v19
	v_max3_f32 v36, |v122|, |v123|, v36
	v_max3_f32 v19, v19, 0, v36
	v_max_f32_e64 v36, |v117|, |v117|
	v_max_f32_e64 v37, |v116|, |v116|
	v_max_f32_e32 v36, v37, v36
	v_max_f32_e64 v37, |v109|, |v109|
	v_max_f32_e64 v38, |v108|, |v108|
	v_max_f32_e32 v37, v38, v37
	v_max3_f32 v36, |v114|, |v115|, v36
	v_max3_f32 v37, |v106|, |v107|, v37
	v_max3_f32 v19, v19, v36, v37
	v_max_f32_e64 v36, |v101|, |v101|
	v_max_f32_e64 v37, |v100|, |v100|
	v_max_f32_e32 v36, v37, v36
	v_max_f32_e64 v37, |v93|, |v93|
	v_max_f32_e64 v38, |v92|, |v92|
	v_max_f32_e32 v37, v38, v37
	v_max3_f32 v36, |v98|, |v99|, v36
	v_max3_f32 v37, |v90|, |v91|, v37
	v_max3_f32 v19, v19, v36, v37
	v_max_f32_e64 v36, |v81|, |v81|
	v_max_f32_e64 v37, |v80|, |v80|
	v_max_f32_e32 v36, v37, v36
	v_max_f32_e64 v37, |v85|, |v85|
	v_max_f32_e64 v38, |v84|, |v84|
	v_max_f32_e32 v37, v38, v37
	v_max3_f32 v36, |v78|, |v79|, v36
	v_max3_f32 v37, |v82|, |v83|, v37
	v_and_or_b32 v2, v2, s44, 48
	v_max3_f32 v36, v19, v36, v37
	v_med3_f32 v19, v2, v21, v20
	v_med3_f32 v20, v2, v22, v21
	v_med3_f32 v21, v2, v23, v22
	v_med3_f32 v22, v2, v24, v23
	v_med3_f32 v23, v2, v25, v24
	v_med3_f32 v24, v2, v26, v25
	v_med3_f32 v25, v2, v27, v26
	v_med3_f32 v26, v2, v28, v27
	v_med3_f32 v27, v2, v29, v28
	v_med3_f32 v28, v2, v30, v29
	v_med3_f32 v29, v2, v31, v30
	v_med3_f32 v30, v2, v32, v31
	v_med3_f32 v31, v2, v33, v32
	v_med3_f32 v32, v2, v34, v33
	v_med3_f32 v33, v2, v18, v34
	v_max_f32_e32 v2, v2, v2
	v_max_f32_e32 v2, v18, v2
	v_and_or_b32 v3, v3, s44, 49
	v_med3_f32 v18, v3, v20, v19
	v_med3_f32 v19, v3, v21, v20
	v_med3_f32 v20, v3, v22, v21
	v_med3_f32 v21, v3, v23, v22
	v_med3_f32 v22, v3, v24, v23
	v_med3_f32 v23, v3, v25, v24
	v_med3_f32 v24, v3, v26, v25
	v_med3_f32 v25, v3, v27, v26
	v_med3_f32 v26, v3, v28, v27
	v_med3_f32 v27, v3, v29, v28
	v_med3_f32 v28, v3, v30, v29
	v_med3_f32 v29, v3, v31, v30
	v_med3_f32 v30, v3, v32, v31
	v_med3_f32 v31, v3, v33, v32
	v_med3_f32 v32, v3, v2, v33
	v_max_f32_e32 v3, v3, v3
	v_max_f32_e32 v2, v2, v3
	v_and_or_b32 v3, v4, s44, 50
	v_med3_f32 v4, v3, v19, v18
	v_med3_f32 v18, v3, v20, v19
	v_med3_f32 v19, v3, v21, v20
	v_med3_f32 v20, v3, v22, v21
	v_med3_f32 v21, v3, v23, v22
	v_med3_f32 v22, v3, v24, v23
	v_med3_f32 v23, v3, v25, v24
	v_med3_f32 v24, v3, v26, v25
	v_med3_f32 v25, v3, v27, v26
	v_med3_f32 v26, v3, v28, v27
	v_med3_f32 v27, v3, v29, v28
	v_med3_f32 v28, v3, v30, v29
	v_med3_f32 v29, v3, v31, v30
	v_med3_f32 v30, v3, v32, v31
	v_med3_f32 v31, v3, v2, v32
	v_max_f32_e32 v3, v3, v3
	v_max_f32_e32 v2, v2, v3
	v_and_or_b32 v3, v5, s44, 51
	v_med3_f32 v4, v3, v18, v4
	v_med3_f32 v5, v3, v19, v18
	v_med3_f32 v18, v3, v20, v19
	v_med3_f32 v19, v3, v21, v20
	v_med3_f32 v20, v3, v22, v21
	v_med3_f32 v21, v3, v23, v22
	v_med3_f32 v22, v3, v24, v23
	v_med3_f32 v23, v3, v25, v24
	v_med3_f32 v24, v3, v26, v25
	v_med3_f32 v25, v3, v27, v26
	v_med3_f32 v26, v3, v28, v27
	v_med3_f32 v27, v3, v29, v28
	v_med3_f32 v28, v3, v30, v29
	v_med3_f32 v29, v3, v31, v30
	v_med3_f32 v30, v3, v2, v31
	v_max_f32_e32 v3, v3, v3
	v_max_f32_e32 v2, v2, v3
	v_and_or_b32 v3, v6, s44, 52
	v_med3_f32 v4, v3, v5, v4
	v_med3_f32 v5, v3, v18, v5
	v_med3_f32 v6, v3, v19, v18
	v_med3_f32 v18, v3, v20, v19
	v_med3_f32 v19, v3, v21, v20
	v_med3_f32 v20, v3, v22, v21
	v_med3_f32 v21, v3, v23, v22
	v_med3_f32 v22, v3, v24, v23
	v_med3_f32 v23, v3, v25, v24
	v_med3_f32 v24, v3, v26, v25
	v_med3_f32 v25, v3, v27, v26
	v_med3_f32 v26, v3, v28, v27
	v_med3_f32 v27, v3, v29, v28
	v_med3_f32 v28, v3, v30, v29
	v_med3_f32 v29, v3, v2, v30
	v_max_f32_e32 v3, v3, v3
	v_max_f32_e32 v2, v2, v3
	v_and_or_b32 v3, v7, s44, 53
	v_med3_f32 v4, v3, v5, v4
	v_med3_f32 v5, v3, v6, v5
	v_med3_f32 v6, v3, v18, v6
	v_med3_f32 v7, v3, v19, v18
	v_med3_f32 v18, v3, v20, v19
	v_med3_f32 v19, v3, v21, v20
	v_med3_f32 v20, v3, v22, v21
	v_med3_f32 v21, v3, v23, v22
	v_med3_f32 v22, v3, v24, v23
	v_med3_f32 v23, v3, v25, v24
	v_med3_f32 v24, v3, v26, v25
	v_med3_f32 v25, v3, v27, v26
	v_med3_f32 v26, v3, v28, v27
	v_med3_f32 v27, v3, v29, v28
	v_med3_f32 v28, v3, v2, v29
	v_max_f32_e32 v3, v3, v3
	v_max_f32_e32 v2, v2, v3
	v_and_or_b32 v3, v8, s44, 54
	v_med3_f32 v4, v3, v5, v4
	v_med3_f32 v5, v3, v6, v5
; DI int crow(int reg, int h) { return (reg & 3) + 8 * (reg >> 2) + 4 * h; }
; template <int CTRL> DI float dpp_max(float v) { return fmaxf(v, __builtin_bit_cast(float, __builtin_amdgcn_mov_dpp(__builtin_bit_cast(int, v), CTRL, 0xf, 0xf, true))); }
; DI float red2_max(float a, float b) {
;     const auto r = __builtin_amdgcn_permlane32_swap(__float_as_uint(a), __float_as_uint(b), false, false); float s = fmaxf(__uint_as_float(r[0]), __uint_as_float(r[1]));
;     const auto q = __builtin_amdgcn_permlane16_swap(__float_as_uint(s), __float_as_uint(s), false, false); s = fmaxf(__uint_as_float(q[0]), __uint_as_float(q[1]));
;     s = dpp_max<0x128>(s); s = dpp_max<0x141>(s); s = dpp_max<0xB1>(s); s = dpp_max<0x4E>(s); return s;
; }
; DI void p8_phase(Frame& F) {
;     ...
;             for (int kt = 0; kt < 4; ++kt) {
;                 if (kt == 2) { trow_finish2(F, q0 * NGWT + gcT, (q0 + 1) * NGWT + gcT, ra, rb); trow_load(F, (q0 + 2) * NGWT + gcT, ra); trow_load(F, (q0 + 3) * NGWT + gcT, rb); }
; #pragma unroll
;                 for (int reg = 0; reg < 16; ++reg) { const unsigned key = (unsigned)(kt * 32 + crow(reg, h)); const float sv = acc[kt][reg];
;                     topk_insert(L, __uint_as_float((__float_as_uint(sv) & ~127u) | key)); }
;             }
	v_med3_f32 v6, v3, v7, v6
	v_med3_f32 v7, v3, v18, v7
	v_med3_f32 v8, v3, v19, v18
	v_med3_f32 v18, v3, v20, v19
	v_med3_f32 v19, v3, v21, v20
	v_med3_f32 v20, v3, v22, v21
	v_med3_f32 v21, v3, v23, v22
	v_med3_f32 v22, v3, v24, v23
	v_med3_f32 v23, v3, v25, v24
	v_med3_f32 v24, v3, v26, v25
	v_med3_f32 v25, v3, v27, v26
	v_med3_f32 v26, v3, v28, v27
	v_med3_f32 v27, v3, v2, v28
	v_max_f32_e32 v3, v3, v3
	v_max_f32_e32 v2, v2, v3
	v_and_or_b32 v3, v9, s44, 55
	v_med3_f32 v4, v3, v5, v4
	v_med3_f32 v5, v3, v6, v5
	v_med3_f32 v6, v3, v7, v6
	v_med3_f32 v7, v3, v8, v7
	v_med3_f32 v8, v3, v18, v8
	v_med3_f32 v9, v3, v19, v18
	v_med3_f32 v18, v3, v20, v19
	v_med3_f32 v19, v3, v21, v20
	v_med3_f32 v20, v3, v22, v21
	v_med3_f32 v21, v3, v23, v22
	v_med3_f32 v22, v3, v24, v23
	v_med3_f32 v23, v3, v25, v24
	v_med3_f32 v24, v3, v26, v25
	v_med3_f32 v25, v3, v27, v26
	v_med3_f32 v26, v3, v2, v27
	v_max_f32_e32 v3, v3, v3
	v_max_f32_e32 v2, v2, v3
	v_and_or_b32 v3, v10, s44, 56
	v_med3_f32 v4, v3, v5, v4
	v_med3_f32 v5, v3, v6, v5
	v_med3_f32 v6, v3, v7, v6
	v_med3_f32 v7, v3, v8, v7
	v_med3_f32 v8, v3, v9, v8
	v_med3_f32 v9, v3, v18, v9
	v_med3_f32 v10, v3, v19, v18
	v_med3_f32 v18, v3, v20, v19
	v_med3_f32 v19, v3, v21, v20
	v_med3_f32 v20, v3, v22, v21
	v_med3_f32 v21, v3, v23, v22
	v_med3_f32 v22, v3, v24, v23
	v_med3_f32 v23, v3, v25, v24
	v_med3_f32 v24, v3, v26, v25
	v_med3_f32 v25, v3, v2, v26
	v_max_f32_e32 v3, v3, v3
	v_max_f32_e32 v2, v2, v3
	v_and_or_b32 v3, v11, s44, 57
	v_permlane32_swap_b32_e32 v36, v35
	v_med3_f32 v4, v3, v5, v4
	v_med3_f32 v5, v3, v6, v5
	v_med3_f32 v6, v3, v7, v6
	v_med3_f32 v7, v3, v8, v7
	v_med3_f32 v8, v3, v9, v8
	v_med3_f32 v9, v3, v10, v9
	v_med3_f32 v10, v3, v18, v10
	v_med3_f32 v11, v3, v19, v18
	v_med3_f32 v18, v3, v20, v19
	v_med3_f32 v19, v3, v21, v20
	v_med3_f32 v20, v3, v22, v21
	v_med3_f32 v21, v3, v23, v22
	v_med3_f32 v22, v3, v24, v23
	v_med3_f32 v23, v3, v25, v24
	v_med3_f32 v24, v3, v2, v25
	v_max_f32_e32 v3, v3, v3
	v_max_f32_e32 v34, v35, v35
	v_max_f32_e32 v35, v36, v36
	v_max_f32_e32 v2, v2, v3
	v_and_or_b32 v3, v12, s44, 58
	v_max_f32_e32 v34, v35, v34
	v_med3_f32 v4, v3, v5, v4
	v_med3_f32 v5, v3, v6, v5
	v_med3_f32 v6, v3, v7, v6
	v_med3_f32 v7, v3, v8, v7
	v_med3_f32 v8, v3, v9, v8
	v_med3_f32 v9, v3, v10, v9
	v_med3_f32 v10, v3, v11, v10
	v_med3_f32 v11, v3, v18, v11
	v_med3_f32 v12, v3, v19, v18
	v_med3_f32 v18, v3, v20, v19
	v_med3_f32 v19, v3, v21, v20
	v_med3_f32 v20, v3, v22, v21
	v_med3_f32 v21, v3, v23, v22
	v_med3_f32 v22, v3, v24, v23
	v_med3_f32 v23, v3, v2, v24
	v_max_f32_e32 v3, v3, v3
	v_mov_b32_e32 v35, v34
	v_max_f32_e32 v2, v2, v3
	v_and_or_b32 v3, v13, s44, 59
	v_permlane16_swap_b32_e32 v34, v35
	v_med3_f32 v4, v3, v5, v4
	v_med3_f32 v5, v3, v6, v5
	v_med3_f32 v6, v3, v7, v6
	v_med3_f32 v7, v3, v8, v7
	v_med3_f32 v8, v3, v9, v8
	v_med3_f32 v9, v3, v10, v9
	v_med3_f32 v10, v3, v11, v10
	v_med3_f32 v11, v3, v12, v11
	v_med3_f32 v12, v3, v18, v12
	v_med3_f32 v13, v3, v19, v18
	v_med3_f32 v18, v3, v20, v19
	v_med3_f32 v19, v3, v21, v20
	v_med3_f32 v20, v3, v22, v21
	v_med3_f32 v21, v3, v23, v22
	v_med3_f32 v22, v3, v2, v23
	v_max_f32_e32 v3, v3, v3
	v_max_f32_e32 v35, v35, v35
	v_max_f32_e32 v34, v34, v34
	v_max_f32_e32 v2, v2, v3
	v_and_or_b32 v3, v14, s44, 60
	v_max_f32_e32 v34, v34, v35
	v_med3_f32 v4, v3, v5, v4
	v_med3_f32 v5, v3, v6, v5
	v_med3_f32 v6, v3, v7, v6
	v_med3_f32 v7, v3, v8, v7
	v_med3_f32 v8, v3, v9, v8
	v_med3_f32 v9, v3, v10, v9
	v_med3_f32 v10, v3, v11, v10
	v_med3_f32 v11, v3, v12, v11
	v_med3_f32 v12, v3, v13, v12
	v_med3_f32 v13, v3, v18, v13
	v_med3_f32 v14, v3, v19, v18
	v_med3_f32 v18, v3, v20, v19
	v_med3_f32 v19, v3, v21, v20
	v_med3_f32 v20, v3, v22, v21
	v_med3_f32 v21, v3, v2, v22
	v_max_f32_e32 v3, v3, v3
	v_mov_b32_dpp v35, v34 row_ror:8 row_mask:0xf bank_mask:0xf bound_ctrl:1
	v_max_f32_e32 v2, v2, v3
	v_and_or_b32 v3, v15, s44, 61
	v_max_f32_e32 v35, v35, v35
	v_med3_f32 v4, v3, v5, v4
	v_med3_f32 v5, v3, v6, v5
	v_med3_f32 v6, v3, v7, v6
	v_med3_f32 v7, v3, v8, v7
	v_med3_f32 v8, v3, v9, v8
	v_med3_f32 v9, v3, v10, v9
	v_med3_f32 v10, v3, v11, v10
	v_med3_f32 v11, v3, v12, v11
	v_med3_f32 v12, v3, v13, v12
	v_med3_f32 v13, v3, v14, v13
	v_med3_f32 v14, v3, v18, v14
	v_med3_f32 v15, v3, v19, v18
	v_med3_f32 v18, v3, v20, v19
	v_med3_f32 v19, v3, v21, v20
	v_med3_f32 v20, v3, v2, v21
	v_max_f32_e32 v3, v3, v3
	v_max_f32_e32 v34, v34, v35
	v_max_f32_e32 v2, v2, v3
	v_and_or_b32 v3, v16, s44, 62
	v_mov_b32_dpp v35, v34 row_half_mirror row_mask:0xf bank_mask:0xf bound_ctrl:1
	v_med3_f32 v4, v3, v5, v4
	v_med3_f32 v5, v3, v6, v5
	v_med3_f32 v6, v3, v7, v6
	v_med3_f32 v7, v3, v8, v7
	v_med3_f32 v8, v3, v9, v8
	v_med3_f32 v9, v3, v10, v9
	v_med3_f32 v10, v3, v11, v10
	v_med3_f32 v11, v3, v12, v11
	v_med3_f32 v12, v3, v13, v12
	v_med3_f32 v13, v3, v14, v13
	v_med3_f32 v14, v3, v15, v14
	v_med3_f32 v15, v3, v18, v15
	v_med3_f32 v16, v3, v19, v18
	v_med3_f32 v31, v3, v20, v19
	v_med3_f32 v32, v3, v2, v20
	v_max_f32_e32 v3, v3, v3
	v_max_f32_e32 v35, v35, v35
	v_max_f32_e32 v2, v2, v3
	v_and_or_b32 v3, v17, s44, 63
	v_max_f32_e32 v34, v34, v35
	v_med3_f32 v18, v3, v5, v4
	v_med3_f32 v19, v3, v6, v5
	v_med3_f32 v20, v3, v7, v6
	v_med3_f32 v21, v3, v8, v7
	v_med3_f32 v22, v3, v9, v8
	v_med3_f32 v23, v3, v10, v9
	v_med3_f32 v24, v3, v11, v10
	v_med3_f32 v25, v3, v12, v11
	v_med3_f32 v26, v3, v13, v12
	v_med3_f32 v27, v3, v14, v13
	v_med3_f32 v28, v3, v15, v14
	v_med3_f32 v29, v3, v16, v15
	v_med3_f32 v30, v3, v31, v16
	v_med3_f32 v31, v3, v32, v31
	v_med3_f32 v32, v3, v2, v32
	v_max_f32_e32 v3, v3, v3
	v_mov_b32_dpp v35, v34 quad_perm:[1,0,3,2] row_mask:0xf bank_mask:0xf bound_ctrl:1
; DI int crow(int reg, int h) { return (reg & 3) + 8 * (reg >> 2) + 4 * h; }
; DI void p8_phase(Frame& F) {
;     ...
;                 for (int reg = 0; reg < 16; ++reg) { const unsigned key = (unsigned)(kt * 32 + crow(reg, h)); const float sv = acc[kt][reg];
;     ...
;             float P[16];
; #pragma unroll
;             for (int i = 0; i < 16; ++i) P[i] = __shfl_xor(L[i], 32);
	v_max_f32_e32 v17, v2, v3
	v_max_f32_e32 v35, v35, v35
	v_and_b32_e32 v147, 60, v17
	v_add3_u32 v17, v17, v147, v131
	v_and_b32_e32 v147, 60, v32
	v_add3_u32 v32, v32, v147, v131
	v_and_b32_e32 v147, 60, v31
	v_add3_u32 v31, v31, v147, v131
	v_and_b32_e32 v147, 60, v30
	v_add3_u32 v30, v30, v147, v131
	v_and_b32_e32 v147, 60, v29
	v_add3_u32 v29, v29, v147, v131
	v_and_b32_e32 v147, 60, v28
	v_add3_u32 v28, v28, v147, v131
	v_and_b32_e32 v147, 60, v27
	v_add3_u32 v27, v27, v147, v131
	v_and_b32_e32 v147, 60, v26
	v_add3_u32 v26, v26, v147, v131
	v_and_b32_e32 v147, 60, v25
	v_add3_u32 v25, v25, v147, v131
	v_and_b32_e32 v147, 60, v24
	v_add3_u32 v24, v24, v147, v131
	v_and_b32_e32 v147, 60, v23
	v_add3_u32 v23, v23, v147, v131
	v_and_b32_e32 v147, 60, v22
	v_add3_u32 v22, v22, v147, v131
	v_and_b32_e32 v147, 60, v21
	v_add3_u32 v21, v21, v147, v131
	v_and_b32_e32 v147, 60, v20
	v_add3_u32 v20, v20, v147, v131
	v_and_b32_e32 v147, 60, v19
	v_add3_u32 v19, v19, v147, v131
	v_and_b32_e32 v147, 60, v18
	v_add3_u32 v18, v18, v147, v131
	ds_bpermute_b32 v33, v137, v17
	ds_bpermute_b32 v15, v137, v32
	ds_bpermute_b32 v14, v137, v31
	ds_bpermute_b32 v13, v137, v30
	ds_bpermute_b32 v12, v137, v29
	ds_bpermute_b32 v11, v137, v28
	ds_bpermute_b32 v10, v137, v27
	ds_bpermute_b32 v9, v137, v26
	ds_bpermute_b32 v8, v137, v25
	ds_bpermute_b32 v7, v137, v24
	ds_bpermute_b32 v6, v137, v23
	ds_bpermute_b32 v5, v137, v22
	ds_bpermute_b32 v4, v137, v21
	ds_bpermute_b32 v3, v137, v20
	ds_bpermute_b32 v2, v137, v19
	ds_bpermute_b32 v16, v137, v18
	v_max_f32_e32 v34, v34, v35
	s_cmpk_gt_i32 s30, 0x7fff
	s_nop 0
	v_mov_b32_dpp v35, v34 quad_perm:[2,3,0,1] row_mask:0xf bank_mask:0xf bound_ctrl:1
	v_max_f32_e32 v35, v35, v35
	v_max_f32_e32 v34, v34, v35
	s_nop 0
	v_readlane_b32 s30, v34, 0
	s_cbranch_scc1 .LBB0_1228
; #define GAS __attribute__((address_space(1)))
; DI void trow_store(Frame& F, int row, const f32x4 (&v)[8], float am) {
;     if (row >= 2 * NEXP) return;
;     const int tb = row >= NEXP, e = row - tb * NEXP; am = fmaxf(am, 1e-30f);
;     const float sc = am * (1.0f / 127.0f), inv = 127.0f / am;
;     GAS unsigned* dst = (GAS unsigned*)((tb ? F.EU : F.ED) + (size_t)e * D) + F.lane;
;     const int off = 0;
; #pragma unroll
;     for (int j = 0; j < 8; ++j) {
;         const int q0 = (int)__builtin_rintf(v[j].x * inv) + off, q1 = (int)__builtin_rintf(v[j].y * inv) + off, q2 = (int)__builtin_rintf(v[j].z * inv) + off, q3 = (int)__builtin_rintf(v[j].w * inv) + off;
;         dst[64 * j] = (unsigned)(q0 & 255) | ((unsigned)(q1 & 255) << 8) | ((unsigned)(q2 & 255) << 16) | ((unsigned)(q3 & 255) << 24);
;     }
;     if (F.lane == 0) (tb ? F.SU : F.SD)[e] = sc;
; }
	s_nop 0
	v_max_f32_e64 v35, s30, s30
	v_max_f32_e32 v35, 0xda24260, v35
	v_div_scale_f32 v36, s[30:31], v35, v35, s42
	v_rcp_f32_e32 v37, v36
	v_div_scale_f32 v38, vcc, s42, v35, s42
	s_and_b64 s[30:31], s[28:29], exec
	v_fma_f32 v39, -v36, v37, 1.0
	v_fmac_f32_e32 v37, v39, v37
	v_mul_f32_e32 v39, v38, v37
	v_fma_f32 v40, -v36, v39, v38
	v_fmac_f32_e32 v39, v40, v37
	v_fma_f32 v36, -v36, v39, v38
	v_div_fmas_f32 v36, v36, v37, v39
	v_div_fixup_f32 v36, v36, v35, s42
	v_mul_f32_e32 v38, v127, v36
	v_mul_f32_e32 v37, v126, v36
	v_rndne_f32_e32 v38, v38
	v_mul_f32_e32 v39, v128, v36
	v_mul_f32_e32 v40, v129, v36
	v_rndne_f32_e32 v37, v37
	v_cvt_i32_f32_e32 v38, v38
	v_rndne_f32_e32 v39, v39
	v_rndne_f32_e32 v40, v40
	v_cvt_i32_f32_e32 v37, v37
	v_cvt_i32_f32_sdwa v39, v39 dst_sel:WORD_1 dst_unused:UNUSED_PAD src0_sel:DWORD
	v_cvt_i32_f32_e32 v40, v40
	s_cselect_b32 s33, s19, s39
	s_cselect_b32 s50, s18, s37
	s_lshl_b64 s[30:31], s[26:27], 11
	v_lshlrev_b32_e32 v38, 8, v38
	s_add_u32 s30, s50, s30
	v_and_b32_e32 v38, 0xff00, v38
	v_and_b32_e32 v39, 0xff0000, v39
	v_perm_b32 v37, v40, v37, s43
	s_addc_u32 s31, s33, s31
	v_or3_b32 v37, v37, v38, v39
	v_mul_f32_e32 v38, v123, v36
	global_store_dword v135, v37, s[30:31]
	v_mul_f32_e32 v37, v122, v36
	v_rndne_f32_e32 v38, v38
	v_mul_f32_e32 v39, v124, v36
	v_mul_f32_e32 v40, v125, v36
	v_rndne_f32_e32 v37, v37
	v_cvt_i32_f32_e32 v38, v38
	v_rndne_f32_e32 v39, v39
	v_rndne_f32_e32 v40, v40
	v_cvt_i32_f32_e32 v37, v37
	v_cvt_i32_f32_sdwa v39, v39 dst_sel:WORD_1 dst_unused:UNUSED_PAD src0_sel:DWORD
	v_cvt_i32_f32_e32 v40, v40
	v_lshlrev_b32_e32 v38, 8, v38
	v_and_b32_e32 v38, 0xff00, v38
	v_and_b32_e32 v39, 0xff0000, v39
	v_perm_b32 v37, v40, v37, s43
	v_or3_b32 v37, v37, v38, v39
	v_mul_f32_e32 v38, v115, v36
	global_store_dword v135, v37, s[30:31] offset:256
	v_mul_f32_e32 v37, v114, v36
	v_rndne_f32_e32 v38, v38
	v_mul_f32_e32 v39, v116, v36
	v_mul_f32_e32 v40, v117, v36
	v_rndne_f32_e32 v37, v37
	v_cvt_i32_f32_e32 v38, v38
	v_rndne_f32_e32 v39, v39
	v_rndne_f32_e32 v40, v40
	v_cvt_i32_f32_e32 v37, v37
	v_cvt_i32_f32_sdwa v39, v39 dst_sel:WORD_1 dst_unused:UNUSED_PAD src0_sel:DWORD
	v_cvt_i32_f32_e32 v40, v40
	v_lshlrev_b32_e32 v38, 8, v38
	v_and_b32_e32 v38, 0xff00, v38
	v_and_b32_e32 v39, 0xff0000, v39
	v_perm_b32 v37, v40, v37, s43
	v_or3_b32 v37, v37, v38, v39
	v_mul_f32_e32 v38, v107, v36
	global_store_dword v135, v37, s[30:31] offset:512
	v_mul_f32_e32 v37, v106, v36
	v_rndne_f32_e32 v38, v38
	v_mul_f32_e32 v39, v108, v36
	v_mul_f32_e32 v40, v109, v36
	v_rndne_f32_e32 v37, v37
	v_cvt_i32_f32_e32 v38, v38
	v_rndne_f32_e32 v39, v39
	v_rndne_f32_e32 v40, v40
	v_cvt_i32_f32_e32 v37, v37
	v_cvt_i32_f32_sdwa v39, v39 dst_sel:WORD_1 dst_unused:UNUSED_PAD src0_sel:DWORD
	v_cvt_i32_f32_e32 v40, v40
	v_lshlrev_b32_e32 v38, 8, v38
	v_and_b32_e32 v38, 0xff00, v38
	v_and_b32_e32 v39, 0xff0000, v39
	v_perm_b32 v37, v40, v37, s43
	v_or3_b32 v37, v37, v38, v39
	v_mul_f32_e32 v38, v99, v36
	global_store_dword v135, v37, s[30:31] offset:768
	v_mul_f32_e32 v37, v98, v36
	v_rndne_f32_e32 v38, v38
	v_mul_f32_e32 v39, v100, v36
	v_mul_f32_e32 v40, v101, v36
	v_rndne_f32_e32 v37, v37
	v_cvt_i32_f32_e32 v38, v38
	v_rndne_f32_e32 v39, v39
	v_rndne_f32_e32 v40, v40
	v_cvt_i32_f32_e32 v37, v37
	v_cvt_i32_f32_sdwa v39, v39 dst_sel:WORD_1 dst_unused:UNUSED_PAD src0_sel:DWORD
	v_cvt_i32_f32_e32 v40, v40
	v_lshlrev_b32_e32 v38, 8, v38
	v_and_b32_e32 v38, 0xff00, v38
	v_and_b32_e32 v39, 0xff0000, v39
	v_perm_b32 v37, v40, v37, s43
	v_or3_b32 v37, v37, v38, v39
	v_mul_f32_e32 v38, v91, v36
	global_store_dword v135, v37, s[30:31] offset:1024
	v_mul_f32_e32 v37, v90, v36
	v_rndne_f32_e32 v38, v38
	v_mul_f32_e32 v39, v92, v36
	v_mul_f32_e32 v40, v93, v36
	v_rndne_f32_e32 v37, v37
	v_cvt_i32_f32_e32 v38, v38
	v_rndne_f32_e32 v39, v39
	v_rndne_f32_e32 v40, v40
	v_cvt_i32_f32_e32 v37, v37
	v_cvt_i32_f32_sdwa v39, v39 dst_sel:WORD_1 dst_unused:UNUSED_PAD src0_sel:DWORD
	v_cvt_i32_f32_e32 v40, v40
	v_lshlrev_b32_e32 v38, 8, v38
	v_and_b32_e32 v38, 0xff00, v38
	v_and_b32_e32 v39, 0xff0000, v39
	v_perm_b32 v37, v40, v37, s43
	v_or3_b32 v37, v37, v38, v39
	v_mul_f32_e32 v38, v79, v36
	global_store_dword v135, v37, s[30:31] offset:1280
	v_mul_f32_e32 v37, v78, v36
	v_rndne_f32_e32 v38, v38
	v_mul_f32_e32 v39, v80, v36
	v_mul_f32_e32 v40, v81, v36
	v_rndne_f32_e32 v37, v37
	v_cvt_i32_f32_e32 v38, v38
	v_rndne_f32_e32 v39, v39
	v_rndne_f32_e32 v40, v40
	v_cvt_i32_f32_e32 v37, v37
	v_cvt_i32_f32_sdwa v39, v39 dst_sel:WORD_1 dst_unused:UNUSED_PAD src0_sel:DWORD
	v_cvt_i32_f32_e32 v40, v40
	v_lshlrev_b32_e32 v38, 8, v38
	v_and_b32_e32 v38, 0xff00, v38
	v_and_b32_e32 v39, 0xff0000, v39
	v_perm_b32 v37, v40, v37, s43
	v_or3_b32 v37, v37, v38, v39
	v_mul_f32_e32 v38, v83, v36
	global_store_dword v135, v37, s[30:31] offset:1536
	v_mul_f32_e32 v37, v82, v36
	v_rndne_f32_e32 v38, v38
	v_mul_f32_e32 v39, v84, v36
	v_mul_f32_e32 v36, v85, v36
	v_rndne_f32_e32 v37, v37
	v_cvt_i32_f32_e32 v38, v38
	v_rndne_f32_e32 v39, v39
	v_rndne_f32_e32 v36, v36
	v_cvt_i32_f32_e32 v37, v37
	v_cvt_i32_f32_sdwa v39, v39 dst_sel:WORD_1 dst_unused:UNUSED_PAD src0_sel:DWORD
	v_cvt_i32_f32_e32 v36, v36
	v_lshlrev_b32_e32 v38, 8, v38
	v_and_b32_e32 v38, 0xff00, v38
	v_and_b32_e32 v39, 0xff0000, v39
	v_perm_b32 v36, v36, v37, s43
	v_or3_b32 v36, v36, v38, v39
	global_store_dword v135, v36, s[30:31] offset:1792
	s_and_saveexec_b64 s[30:31], s[4:5]
	s_cbranch_execz .LBB0_1227
	s_and_b64 s[28:29], s[28:29], exec
	s_cselect_b32 s28, s25, s21
	s_cselect_b32 s29, s24, s20
	s_lshl_b64 s[26:27], s[26:27], 2
	s_add_u32 s26, s29, s26
	s_addc_u32 s27, s28, s27
	v_mul_f32_e32 v35, 0x3c010204, v35
	global_store_dword v133, v35, s[26:27]
